# k_layer<2>: parallel instruction-cache warm-up - branch pads every 14 instrs in the task loop, each wave hops through 1/16 of them during the prologue load latency
# speedup vs baseline: 1.1794x; 1.0903x over previous
.LBB5_10:
	v_lshrrev_b32_e32 v2, 3, v0
	s_load_dwordx2 s[30:31], s[0:1], 0x40
	v_and_b32_e32 v1, 63, v0
	v_and_b32_e32 v2, 0x78, v2
	s_movk_i32 s2, 0xa0
	v_bfe_u32 v74, v0, 3, 3
	v_and_b32_e32 v75, 7, v0
	v_and_b32_e32 v77, 15, v0
	s_sub_i32 s0, s28, s20
	v_and_b32_e32 v5, 48, v0
	v_lshrrev_b32_e32 v0, 2, v0
	v_mad_u32_u24 v2, v2, s2, 0
	s_add_i32 s0, s0, 7
	v_mul_u32_u24_e32 v4, 0xa0, v75
	v_and_b32_e32 v0, 12, v0
	v_lshlrev_b32_e32 v76, 4, v75
	s_ashr_i32 s21, s0, 3
	v_cmp_eq_u32_e64 s[0:1], 0, v1
	v_mad_u32_u24 v3, v74, s2, v2
	v_add3_u32 v80, v2, v4, v5
	v_add_u32_e32 v2, 0, v5
	v_cmp_gt_u32_e64 s[4:5], 16, v1
	v_mul_u32_u24_e32 v1, 0x220, v77
	v_lshlrev_b32_e32 v32, 2, v0
	v_mbcnt_lo_u32_b32 v0, -1, 0
	v_mov_b32_e32 v33, 0
	v_or_b32_e32 v78, 8, v75
	v_or_b32_e32 v79, 16, v75
	v_lshlrev_b32_e32 v81, 3, v75
	v_cmp_gt_u32_e64 s[2:3], 8, v77
	s_mov_b32 s29, 0x3c800000
	v_add_u32_e32 v82, v3, v76
	v_add_u32_e32 v83, v2, v1
	v_add_u32_e32 v83, 0xcf10, v83
	v_mbcnt_hi_u32_b32 v84, -1, v0
	s_lshl_b32 s33, s38, 3
	s_add_i32 s33, s33, s20
	v_add_u32_e32 v8, s33, v74
	v_cmp_gt_i32_e32 vcc, s28, v8
	v_mov_b32_e32 v0, 0
	v_mov_b32_e32 v1, 0
	v_mov_b32_e32 v2, 0
	v_mov_b32_e32 v3, 0
	v_mov_b32_e32 v4, 0
	v_mov_b32_e32 v5, 0
	v_mov_b32_e32 v6, 0
	v_mov_b32_e32 v7, 0
	s_and_saveexec_b64 s[6:7], vcc
	v_lshl_add_u32 v9, v8, 1, v8
	v_lshlrev_b32_e32 v9, 2, v9
	global_load_dwordx4 v[4:7], v9, s[14:15]
	v_lshl_or_b32 v9, v8, 7, v76
	global_load_dwordx4 v[0:3], v9, s[12:13]
	s_mov_b64 exec, s[6:7]
	s_cmp_eq_u32 s38, 0
	s_cbranch_scc1 .Lic2_t0
	s_cmp_eq_u32 s38, 1
	s_cbranch_scc1 .Lic2_t1
	s_cmp_eq_u32 s38, 2
	s_cbranch_scc1 .Lic2_t2
	s_cmp_eq_u32 s38, 3
	s_cbranch_scc1 .Lic2_t3
	s_cmp_eq_u32 s38, 4
	s_cbranch_scc1 .Lic2_t4
	s_cmp_eq_u32 s38, 5
	s_cbranch_scc1 .Lic2_t5
	s_cmp_eq_u32 s38, 6
	s_cbranch_scc1 .Lic2_t6
	s_cmp_eq_u32 s38, 7
	s_cbranch_scc1 .Lic2_t7
	s_cmp_eq_u32 s38, 8
	s_cbranch_scc1 .Lic2_t8
	s_cmp_eq_u32 s38, 9
	s_cbranch_scc1 .Lic2_t9
	s_cmp_eq_u32 s38, 10
	s_cbranch_scc1 .Lic2_t10
	s_cmp_eq_u32 s38, 11
	s_cbranch_scc1 .Lic2_t11
	s_cmp_eq_u32 s38, 12
	s_cbranch_scc1 .Lic2_t12
	s_cmp_eq_u32 s38, 13
	s_cbranch_scc1 .Lic2_t13
	s_cmp_eq_u32 s38, 14
	s_cbranch_scc1 .Lic2_t14
	s_cmp_eq_u32 s38, 15
	s_cbranch_scc1 .Lic2_t15
.Lic2_done:
	s_waitcnt vmcnt(3)
	ds_write_b128 v20, v[22:25]
	s_waitcnt vmcnt(2)
	ds_write_b128 v20, v[26:29] offset:17408
	s_and_saveexec_b64 s[6:7], s[40:41]
	ds_write_b128 v14, v[16:19] offset:52240
	s_mov_b64 exec, s[6:7]
	s_waitcnt vmcnt(1)
	v_sub_u32_e32 v58, v5, v4
	v_sub_u32_e32 v87, v6, v5
	v_sub_u32_e32 v85, v7, v6
	v_add_lshl_u32 v10, v4, v75, 2
	v_add_lshl_u32 v11, v5, v75, 2
	v_add_lshl_u32 v12, v6, v75, 2
	v_mov_b32_e32 v9, 0x186a0
	v_mov_b32_e32 v8, 0x186a0
	v_mov_b32_e32 v60, 0x186a0
	v_mov_b32_e32 v59, 0x186a0
	v_mov_b32_e32 v62, 0x186a0
	v_mov_b32_e32 v89, 0x186a0
	v_mov_b32_e32 v88, 0x186a0
	v_mov_b32_e32 v86, 0x186a0
	v_mov_b32_e32 v7, 0x186a0
	s_mov_b64 s[6:7], exec
	v_cmp_lt_i32_e32 vcc, v75, v58
	s_and_b64 exec, exec, vcc
	global_load_dword v9, v10, s[26:27]
	v_cmp_lt_i32_e32 vcc, v78, v58
	s_and_b64 exec, exec, vcc
	global_load_dword v8, v10, s[26:27] offset:32
	v_cmp_lt_i32_e32 vcc, v79, v58
	s_and_b64 exec, exec, vcc
	global_load_dword v60, v10, s[26:27] offset:64
	s_mov_b64 exec, s[6:7]
	v_cmp_lt_i32_e32 vcc, v75, v87
	s_and_b64 exec, exec, vcc
	global_load_dword v59, v11, s[26:27]
	v_cmp_lt_i32_e32 vcc, v78, v87
	s_and_b64 exec, exec, vcc
	global_load_dword v62, v11, s[26:27] offset:32
	v_cmp_lt_i32_e32 vcc, v79, v87
	s_and_b64 exec, exec, vcc
	global_load_dword v89, v11, s[26:27] offset:64
	s_mov_b64 exec, s[6:7]
	v_cmp_lt_i32_e32 vcc, v75, v85
	s_and_b64 exec, exec, vcc
	global_load_dword v88, v12, s[26:27]
	v_cmp_lt_i32_e32 vcc, v78, v85
	s_and_b64 exec, exec, vcc
	global_load_dword v86, v12, s[26:27] offset:32
	v_cmp_lt_i32_e32 vcc, v79, v85
	s_and_b64 exec, exec, vcc
	global_load_dword v7, v12, s[26:27] offset:64
	s_mov_b64 exec, s[6:7]
	s_waitcnt lgkmcnt(0)
	s_barrier
	s_cmp_ge_i32 s38, s21
	s_cbranch_scc1 .LBB5_118
	s_branch .Lp2_after_idx

.LBB5_13:
	s_waitcnt lgkmcnt(0)
	v_mov_b32_e32 v0, 0
	s_and_saveexec_b64 s[6:7], s[0:1]
	s_cbranch_execz .LBB5_17
	s_mov_b64 s[10:11], exec
	v_mbcnt_lo_u32_b32 v0, s10, 0
	v_mbcnt_hi_u32_b32 v0, s11, v0
	v_cmp_eq_u32_e32 vcc, 0, v0
	s_and_saveexec_b64 s[8:9], vcc
	s_bcnt1_i32_b64 s10, s[10:11]
	v_mov_b32_e32 v1, s10
	ds_add_rtn_u32 v1, v33, v1 offset:52224
	s_or_b64 exec, exec, s[8:9]
	s_waitcnt lgkmcnt(0)
	s_branch .Lic2_s0

.Lic2_s0:
	v_readfirstlane_b32 s8, v1
	s_nop 1
	v_add_u32_e32 v0, s8, v0
.LBB5_17:
	s_or_b64 exec, exec, s[6:7]
	v_readfirstlane_b32 s8, v0
	s_cmp_ge_i32 s8, s21
	s_mov_b64 s[6:7], -1
	s_cbranch_scc1 .LBB5_12
	s_lshl_b32 s33, s8, 3
	s_add_i32 s33, s33, s20
	v_add_u32_e32 v8, s33, v74
	v_cmp_gt_i32_e32 vcc, s28, v8
	v_mov_b32_e32 v0, 0
	v_mov_b32_e32 v6, 0
	s_branch .Lic2_s1

.Lic2_s1:
	v_mov_b32_e32 v7, 0
	v_mov_b32_e32 v4, 0
	v_mov_b32_e32 v5, 0
	s_and_saveexec_b64 s[6:7], vcc
	s_cbranch_execz .LBB5_20
	v_lshl_add_u32 v2, v8, 1, v8
	v_ashrrev_i32_e32 v3, 31, v2
	v_lshl_add_u64 v[2:3], v[2:3], 2, s[14:15]
	global_load_dwordx4 v[4:7], v[2:3], off
.LBB5_20:
	s_or_b64 exec, exec, s[6:7]
	v_mov_b32_e32 v1, 0
	v_mov_b32_e32 v2, 0
	v_mov_b32_e32 v3, 0
	s_and_saveexec_b64 s[6:7], vcc
	s_branch .Lic2_s2

.Lic2_s2:
	s_cbranch_execz .LBB5_22
	v_lshl_or_b32 v0, v8, 7, v76
	global_load_dwordx4 v[0:3], v0, s[12:13]
.LBB5_22:
	s_or_b64 exec, exec, s[6:7]
	s_waitcnt vmcnt(1)
	v_sub_u32_e32 v58, v5, v4
	v_sub_u32_e32 v87, v6, v5
	v_sub_u32_e32 v85, v7, v6
	v_add_lshl_u32 v10, v4, v75, 2
	v_add_lshl_u32 v11, v5, v75, 2
	v_add_lshl_u32 v12, v6, v75, 2
	v_mov_b32_e32 v9, 0x186a0
	v_mov_b32_e32 v8, 0x186a0
	v_mov_b32_e32 v60, 0x186a0
	s_branch .Lic2_s3

.Lic2_s3:
	v_mov_b32_e32 v59, 0x186a0
	v_mov_b32_e32 v62, 0x186a0
	v_mov_b32_e32 v89, 0x186a0
	v_mov_b32_e32 v88, 0x186a0
	v_mov_b32_e32 v86, 0x186a0
	v_mov_b32_e32 v7, 0x186a0
	s_mov_b64 s[6:7], exec
	v_cmp_lt_i32_e32 vcc, v75, v58
	s_and_b64 exec, exec, vcc
	global_load_dword v9, v10, s[26:27]
	v_cmp_lt_i32_e32 vcc, v78, v58
	s_and_b64 exec, exec, vcc
	global_load_dword v8, v10, s[26:27] offset:32
	v_cmp_lt_i32_e32 vcc, v79, v58
	s_branch .Lic2_s4

.Lic2_s4:
	s_and_b64 exec, exec, vcc
	global_load_dword v60, v10, s[26:27] offset:64
	s_mov_b64 exec, s[6:7]
	v_cmp_lt_i32_e32 vcc, v75, v87
	s_and_b64 exec, exec, vcc
	global_load_dword v59, v11, s[26:27]
	v_cmp_lt_i32_e32 vcc, v78, v87
	s_and_b64 exec, exec, vcc
	global_load_dword v62, v11, s[26:27] offset:32
	v_cmp_lt_i32_e32 vcc, v79, v87
	s_and_b64 exec, exec, vcc
	global_load_dword v89, v11, s[26:27] offset:64
	s_mov_b64 exec, s[6:7]
	v_cmp_lt_i32_e32 vcc, v75, v85
	s_branch .Lic2_s5

.Lic2_s5:
	s_and_b64 exec, exec, vcc
	global_load_dword v88, v12, s[26:27]
	v_cmp_lt_i32_e32 vcc, v78, v85
	s_and_b64 exec, exec, vcc
	global_load_dword v86, v12, s[26:27] offset:32
	v_cmp_lt_i32_e32 vcc, v79, v85
	s_and_b64 exec, exec, vcc
	global_load_dword v7, v12, s[26:27] offset:64
	s_mov_b64 exec, s[6:7]
.Lp2_after_idx:
	v_add_u32_e32 v102, s33, v77
	v_cmp_gt_i32_e32 vcc, s28, v102
	v_mov_b32_e32 v103, -1
	s_and_b64 s[8:9], s[2:3], vcc
	s_mov_b64 s[6:7], exec
	s_branch .Lic2_s6

.Lic2_s6:
	s_and_b64 exec, exec, s[8:9]
	v_lshlrev_b32_e32 v102, 2, v102
	global_load_dword v103, v102, s[16:17]
	s_mov_b64 exec, s[6:7]
	s_waitcnt vmcnt(0)
	v_lshlrev_b32_e32 v9, 6, v9
	v_lshlrev_b32_e32 v8, 6, v8
	v_lshlrev_b32_e32 v60, 6, v60
	v_lshlrev_b32_e32 v59, 6, v59
	v_lshlrev_b32_e32 v62, 6, v62
	v_lshlrev_b32_e32 v89, 6, v89
	v_lshlrev_b32_e32 v88, 6, v88
	v_lshlrev_b32_e32 v86, 6, v86
	v_lshlrev_b32_e32 v7, 6, v7
	s_branch .Lic2_s7

.Lic2_s7:
	v_and_b32_e32 v9, 0x7fffc0, v9
	v_and_b32_e32 v8, 0x7fffc0, v8
	v_and_b32_e32 v60, 0x7fffc0, v60
	v_and_b32_e32 v59, 0x7fffc0, v59
	v_and_b32_e32 v62, 0x7fffc0, v62
	v_and_b32_e32 v89, 0x7fffc0, v89
	v_and_b32_e32 v88, 0x7fffc0, v88
	v_and_b32_e32 v86, 0x7fffc0, v86
	v_and_b32_e32 v7, 0x7fffc0, v7
	v_mov_b32_dpp v12, v9 row_newbcast:2 row_mask:0xf bank_mask:0x3
	v_mov_b32_dpp v12, v9 row_newbcast:10 row_mask:0xf bank_mask:0xc
	v_mov_b32_dpp v14, v9 row_newbcast:4 row_mask:0xf bank_mask:0x3
	v_mov_b32_dpp v14, v9 row_newbcast:12 row_mask:0xf bank_mask:0xc
	v_mov_b32_dpp v15, v9 row_newbcast:5 row_mask:0xf bank_mask:0x3
	s_branch .Lic2_s8

.Lic2_s8:
	v_mov_b32_dpp v15, v9 row_newbcast:13 row_mask:0xf bank_mask:0xc
	v_add_u32_dpp v10, v9, v81 row_newbcast:0 row_mask:0xf bank_mask:0x3
	v_add_u32_dpp v10, v9, v81 row_newbcast:8 row_mask:0xf bank_mask:0xc
	v_add_u32_dpp v11, v9, v81 row_newbcast:1 row_mask:0xf bank_mask:0x3
	v_add_u32_dpp v11, v9, v81 row_newbcast:9 row_mask:0xf bank_mask:0xc
	v_add_u32_dpp v13, v9, v81 row_newbcast:3 row_mask:0xf bank_mask:0x3
	v_add_u32_dpp v13, v9, v81 row_newbcast:11 row_mask:0xf bank_mask:0xc
	v_mov_b32_dpp v16, v9 row_newbcast:6 row_mask:0xf bank_mask:0x3
	v_mov_b32_dpp v16, v9 row_newbcast:14 row_mask:0xf bank_mask:0xc
	v_mov_b32_dpp v9, v9 row_newbcast:7 row_mask:0xf bank_mask:0x3
	s_nop 1
	v_mov_b32_dpp v9, v9 row_newbcast:15 row_mask:0xf bank_mask:0xc
	v_add_u32_e32 v12, v12, v81
	global_load_dwordx2 v[56:57], v10, s[30:31]
	s_branch .Lic2_s9

.Lic2_s9:
	global_load_dwordx2 v[52:53], v11, s[30:31]
	global_load_dwordx2 v[30:31], v12, s[30:31]
	global_load_dwordx2 v[24:25], v13, s[30:31]
	v_add_u32_e32 v10, v14, v81
	v_add_u32_e32 v11, v15, v81
	v_add_u32_e32 v9, v9, v81
	v_add_u32_e32 v12, v16, v81
	v_mov_b32_dpp v16, v8 row_newbcast:3 row_mask:0xf bank_mask:0x3
	v_mov_b32_dpp v16, v8 row_newbcast:11 row_mask:0xf bank_mask:0xc
	global_load_dwordx2 v[54:55], v10, s[30:31]
	global_load_dwordx2 v[50:51], v11, s[30:31]
	global_load_dwordx2 v[26:27], v12, s[30:31]
	global_load_dwordx2 v[20:21], v9, s[30:31]
	v_add_u32_dpp v9, v8, v81 row_newbcast:0 row_mask:0xf bank_mask:0x3
	s_branch .Lic2_s10

.Lic2_s10:
	v_add_u32_dpp v9, v8, v81 row_newbcast:8 row_mask:0xf bank_mask:0xc
	v_add_u32_dpp v10, v8, v81 row_newbcast:1 row_mask:0xf bank_mask:0x3
	v_add_u32_dpp v10, v8, v81 row_newbcast:9 row_mask:0xf bank_mask:0xc
	v_add_u32_dpp v11, v8, v81 row_newbcast:2 row_mask:0xf bank_mask:0x3
	v_add_u32_dpp v11, v8, v81 row_newbcast:10 row_mask:0xf bank_mask:0xc
	v_mov_b32_dpp v13, v8 row_newbcast:4 row_mask:0xf bank_mask:0x3
	v_mov_b32_dpp v13, v8 row_newbcast:12 row_mask:0xf bank_mask:0xc
	v_mov_b32_dpp v14, v8 row_newbcast:5 row_mask:0xf bank_mask:0x3
	v_mov_b32_dpp v14, v8 row_newbcast:13 row_mask:0xf bank_mask:0xc
	v_mov_b32_dpp v15, v8 row_newbcast:6 row_mask:0xf bank_mask:0x3
	v_mov_b32_dpp v15, v8 row_newbcast:14 row_mask:0xf bank_mask:0xc
	v_mov_b32_dpp v8, v8 row_newbcast:7 row_mask:0xf bank_mask:0x3
	s_nop 1
	v_mov_b32_dpp v8, v8 row_newbcast:15 row_mask:0xf bank_mask:0xc
	s_branch .Lic2_s11

.Lic2_s11:
	v_add_u32_e32 v12, v16, v81
	global_load_dwordx2 v[28:29], v9, s[30:31]
	global_load_dwordx2 v[22:23], v10, s[30:31]
	global_load_dwordx2 v[18:19], v11, s[30:31]
	global_load_dwordx2 v[16:17], v12, s[30:31]
	v_add_u32_e32 v9, v13, v81
	v_add_u32_e32 v10, v14, v81
	v_add_u32_e32 v11, v15, v81
	v_add_u32_e32 v8, v8, v81
	global_load_dwordx2 v[14:15], v9, s[30:31]
	global_load_dwordx2 v[12:13], v10, s[30:31]
	s_nop 0
	global_load_dwordx2 v[10:11], v11, s[30:31]
	s_nop 0
	s_branch .Lic2_s12

.Lic2_s12:
	global_load_dwordx2 v[8:9], v8, s[30:31]
	v_cmp_lt_i32_e32 vcc, 16, v58
	s_cmp_lg_u64 vcc, 0
	s_cselect_b64 s[36:37], -1, 0
	v_cmp_lt_i32_e64 s[10:11], 18, v58
	v_cmp_lt_i32_e64 s[8:9], 20, v58
	v_cmp_lt_i32_e64 s[6:7], 22, v58
	s_cbranch_vccz .LBB5_42
	v_add_u32_dpp v34, v60, v81 row_newbcast:0 row_mask:0xf bank_mask:0x3
	v_add_u32_dpp v34, v60, v81 row_newbcast:8 row_mask:0xf bank_mask:0xc
	v_add_u32_dpp v38, v60, v81 row_newbcast:1 row_mask:0xf bank_mask:0x3
	v_add_u32_dpp v38, v60, v81 row_newbcast:9 row_mask:0xf bank_mask:0xc
	global_load_dwordx2 v[34:35], v34, s[30:31]
	s_nop 0
	s_branch .Lic2_s13

.Lic2_s13:
	global_load_dwordx2 v[38:39], v38, s[30:31]

.LBB5_44:
	s_cmp_lg_u64 s[8:9], 0
	s_cselect_b64 s[10:11], -1, 0
	s_branch .Lic2_s14

.Lic2_s14:
	s_cmp_eq_u64 s[8:9], 0
	s_cbranch_scc1 .LBB5_46
	v_add_u32_dpp v40, v60, v81 row_newbcast:4 row_mask:0xf bank_mask:0x3
	v_add_u32_dpp v40, v60, v81 row_newbcast:12 row_mask:0xf bank_mask:0xc
	v_add_u32_dpp v46, v60, v81 row_newbcast:5 row_mask:0xf bank_mask:0x3
	v_add_u32_dpp v46, v60, v81 row_newbcast:13 row_mask:0xf bank_mask:0xc
	global_load_dwordx2 v[40:41], v40, s[30:31]
	s_nop 0
	global_load_dwordx2 v[46:47], v46, s[30:31]
.LBB5_46:
	s_cmp_lg_u64 s[6:7], 0
	s_cselect_b64 s[8:9], -1, 0
	s_cmp_eq_u64 s[6:7], 0
	s_cbranch_scc1 .LBB5_48
	v_add_u32_dpp v44, v60, v81 row_newbcast:6 row_mask:0xf bank_mask:0x3
	s_branch .Lic2_s15

.Lic2_s15:
	v_add_u32_dpp v44, v60, v81 row_newbcast:14 row_mask:0xf bank_mask:0xc
	v_add_u32_dpp v48, v60, v81 row_newbcast:7 row_mask:0xf bank_mask:0x3
	v_add_u32_dpp v48, v60, v81 row_newbcast:15 row_mask:0xf bank_mask:0xc
	global_load_dwordx2 v[44:45], v44, s[30:31]
	s_nop 0
	global_load_dwordx2 v[48:49], v48, s[30:31]
.LBB5_48:
	v_cvt_f32_i32_e32 v60, v58
	s_waitcnt vmcnt(15)
	v_cvt_scalef32_pk_f16_fp8 v64, v56, 1.0
	v_cvt_scalef32_pk_f16_fp8 v56, v56, 1.0 op_sel:[1,0,0]
	v_max_f32_e32 v60, 1.0, v60
	v_div_scale_f32 v61, s[6:7], v60, v60, 1.0
	v_rcp_f32_e32 v63, v61
	v_div_scale_f32 v65, vcc, 1.0, v60, 1.0
	s_branch .Lic2_s16

.Lic2_s16:
	v_fma_f32 v66, -v61, v63, 1.0
	v_fmac_f32_e32 v63, v66, v63
	v_mul_f32_e32 v66, v65, v63
	v_fma_f32 v67, -v61, v66, v65
	v_fmac_f32_e32 v66, v67, v63
	v_fma_f32 v61, -v61, v66, v65
	v_div_fmas_f32 v61, v61, v63, v66
	v_div_fixup_f32 v60, v61, v60, 1.0
	v_mul_f32_e32 v61, 0x3c800000, v60
	v_fma_mixlo_f16 v63, v60, s29, 0
	v_cvt_pk_f16_f32 v60, v61, v61
	v_cvt_scalef32_pk_f16_fp8 v61, v57, 1.0
	v_cvt_scalef32_pk_f16_fp8 v57, v57, 1.0 op_sel:[1,0,0]
	v_pk_fma_f16 v64, v63, v64, 0 op_sel_hi:[0,1,1]
	s_branch .Lic2_s17

.Lic2_s17:
	v_pk_fma_f16 v56, v63, v56, 0 op_sel_hi:[0,1,1]
	v_pk_fma_f16 v61, v63, v61, 0 op_sel_hi:[0,1,1]
	v_pk_fma_f16 v57, v63, v57, 0 op_sel_hi:[0,1,1]
	s_waitcnt vmcnt(14)
	v_cvt_scalef32_pk_f16_fp8 v65, v52, 1.0
	v_cvt_scalef32_pk_f16_fp8 v52, v52, 1.0 op_sel:[1,0,0]
	v_cvt_scalef32_pk_f16_fp8 v66, v53, 1.0
	v_cvt_scalef32_pk_f16_fp8 v53, v53, 1.0 op_sel:[1,0,0]
	v_pk_fma_f16 v53, v63, v53, v57 op_sel_hi:[0,1,1]
	v_pk_fma_f16 v57, v63, v66, v61 op_sel_hi:[0,1,1]
	v_pk_fma_f16 v52, v63, v52, v56 op_sel_hi:[0,1,1]
	v_pk_fma_f16 v56, v63, v65, v64 op_sel_hi:[0,1,1]
	s_waitcnt vmcnt(13)
	v_cvt_scalef32_pk_f16_fp8 v61, v30, 1.0
	s_branch .Lic2_s18

.Lic2_s18:
	v_cvt_scalef32_pk_f16_fp8 v30, v30, 1.0 op_sel:[1,0,0]
	v_cvt_scalef32_pk_f16_fp8 v64, v31, 1.0
	v_cvt_scalef32_pk_f16_fp8 v31, v31, 1.0 op_sel:[1,0,0]
	v_pk_fma_f16 v56, v63, v61, v56 op_sel_hi:[0,1,1]
	v_pk_fma_f16 v30, v63, v30, v52 op_sel_hi:[0,1,1]
	v_pk_fma_f16 v52, v63, v64, v57 op_sel_hi:[0,1,1]
	v_pk_fma_f16 v31, v63, v31, v53 op_sel_hi:[0,1,1]
	s_waitcnt vmcnt(12)
	v_cvt_scalef32_pk_f16_fp8 v53, v24, 1.0
	v_cvt_scalef32_pk_f16_fp8 v24, v24, 1.0 op_sel:[1,0,0]
	v_cvt_scalef32_pk_f16_fp8 v57, v25, 1.0
	v_cvt_scalef32_pk_f16_fp8 v25, v25, 1.0 op_sel:[1,0,0]
	v_pk_fma_f16 v25, v63, v25, v31 op_sel_hi:[0,1,1]
	v_pk_fma_f16 v31, v63, v57, v52 op_sel_hi:[0,1,1]
	s_branch .Lic2_s19

.Lic2_s19:
	v_pk_fma_f16 v24, v63, v24, v30 op_sel_hi:[0,1,1]
	v_pk_fma_f16 v30, v63, v53, v56 op_sel_hi:[0,1,1]
	s_waitcnt vmcnt(11)
	v_cvt_scalef32_pk_f16_fp8 v52, v54, 1.0
	v_cvt_scalef32_pk_f16_fp8 v53, v54, 1.0 op_sel:[1,0,0]
	v_cvt_scalef32_pk_f16_fp8 v54, v55, 1.0
	v_cvt_scalef32_pk_f16_fp8 v55, v55, 1.0 op_sel:[1,0,0]
	v_pk_fma_f16 v30, v63, v52, v30 op_sel_hi:[0,1,1]
	v_pk_fma_f16 v24, v63, v53, v24 op_sel_hi:[0,1,1]
	v_pk_fma_f16 v31, v63, v54, v31 op_sel_hi:[0,1,1]
	v_pk_fma_f16 v25, v63, v55, v25 op_sel_hi:[0,1,1]
	s_waitcnt vmcnt(10)
	v_cvt_scalef32_pk_f16_fp8 v52, v50, 1.0
	v_cvt_scalef32_pk_f16_fp8 v50, v50, 1.0 op_sel:[1,0,0]
	s_branch .Lic2_s20

.Lic2_s20:
	v_cvt_scalef32_pk_f16_fp8 v53, v51, 1.0
	v_cvt_scalef32_pk_f16_fp8 v51, v51, 1.0 op_sel:[1,0,0]
	v_pk_fma_f16 v25, v63, v51, v25 op_sel_hi:[0,1,1]
	v_pk_fma_f16 v31, v63, v53, v31 op_sel_hi:[0,1,1]
	v_pk_fma_f16 v24, v63, v50, v24 op_sel_hi:[0,1,1]
	v_pk_fma_f16 v30, v63, v52, v30 op_sel_hi:[0,1,1]
	s_waitcnt vmcnt(9)
	v_cvt_scalef32_pk_f16_fp8 v50, v26, 1.0
	v_cvt_scalef32_pk_f16_fp8 v26, v26, 1.0 op_sel:[1,0,0]
	v_cvt_scalef32_pk_f16_fp8 v51, v27, 1.0
	v_cvt_scalef32_pk_f16_fp8 v27, v27, 1.0 op_sel:[1,0,0]
	v_pk_fma_f16 v30, v63, v50, v30 op_sel_hi:[0,1,1]
	v_pk_fma_f16 v24, v63, v26, v24 op_sel_hi:[0,1,1]
	v_pk_fma_f16 v26, v63, v51, v31 op_sel_hi:[0,1,1]
	s_branch .Lic2_s21

.Lic2_s21:
	v_pk_fma_f16 v25, v63, v27, v25 op_sel_hi:[0,1,1]
	s_waitcnt vmcnt(8)
	v_cvt_scalef32_pk_f16_fp8 v27, v20, 1.0
	v_cvt_scalef32_pk_f16_fp8 v20, v20, 1.0 op_sel:[1,0,0]
	v_cvt_scalef32_pk_f16_fp8 v31, v21, 1.0
	v_cvt_scalef32_pk_f16_fp8 v21, v21, 1.0 op_sel:[1,0,0]
	v_pk_fma_f16 v21, v63, v21, v25 op_sel_hi:[0,1,1]
	v_pk_fma_f16 v25, v63, v31, v26 op_sel_hi:[0,1,1]
	v_pk_fma_f16 v20, v63, v20, v24 op_sel_hi:[0,1,1]
	v_pk_fma_f16 v24, v63, v27, v30 op_sel_hi:[0,1,1]
	s_waitcnt vmcnt(7)
	v_cvt_scalef32_pk_f16_fp8 v26, v28, 1.0
	v_cvt_scalef32_pk_f16_fp8 v27, v28, 1.0 op_sel:[1,0,0]
	v_cvt_scalef32_pk_f16_fp8 v28, v29, 1.0
	s_branch .Lic2_s22

.Lic2_s22:
	v_cvt_scalef32_pk_f16_fp8 v29, v29, 1.0 op_sel:[1,0,0]
	v_pk_fma_f16 v24, v63, v26, v24 op_sel_hi:[0,1,1]
	v_pk_fma_f16 v20, v63, v27, v20 op_sel_hi:[0,1,1]
	v_pk_fma_f16 v25, v63, v28, v25 op_sel_hi:[0,1,1]
	v_pk_fma_f16 v21, v63, v29, v21 op_sel_hi:[0,1,1]
	s_waitcnt vmcnt(6)
	v_cvt_scalef32_pk_f16_fp8 v26, v22, 1.0
	v_cvt_scalef32_pk_f16_fp8 v22, v22, 1.0 op_sel:[1,0,0]
	v_cvt_scalef32_pk_f16_fp8 v27, v23, 1.0
	v_cvt_scalef32_pk_f16_fp8 v23, v23, 1.0 op_sel:[1,0,0]
	v_pk_fma_f16 v21, v63, v23, v21 op_sel_hi:[0,1,1]
	v_pk_fma_f16 v23, v63, v27, v25 op_sel_hi:[0,1,1]
	v_pk_fma_f16 v20, v63, v22, v20 op_sel_hi:[0,1,1]
	v_pk_fma_f16 v22, v63, v26, v24 op_sel_hi:[0,1,1]
	s_branch .Lic2_s23

.Lic2_s23:
	s_waitcnt vmcnt(5)
	v_cvt_scalef32_pk_f16_fp8 v24, v18, 1.0
	v_cvt_scalef32_pk_f16_fp8 v18, v18, 1.0 op_sel:[1,0,0]
	v_cvt_scalef32_pk_f16_fp8 v25, v19, 1.0
	v_cvt_scalef32_pk_f16_fp8 v19, v19, 1.0 op_sel:[1,0,0]
	v_pk_fma_f16 v22, v63, v24, v22 op_sel_hi:[0,1,1]
	v_pk_fma_f16 v18, v63, v18, v20 op_sel_hi:[0,1,1]
	v_pk_fma_f16 v20, v63, v25, v23 op_sel_hi:[0,1,1]
	v_pk_fma_f16 v19, v63, v19, v21 op_sel_hi:[0,1,1]
	s_waitcnt vmcnt(4)
	v_cvt_scalef32_pk_f16_fp8 v21, v16, 1.0
	v_cvt_scalef32_pk_f16_fp8 v16, v16, 1.0 op_sel:[1,0,0]
	v_cvt_scalef32_pk_f16_fp8 v23, v17, 1.0
	v_cvt_scalef32_pk_f16_fp8 v17, v17, 1.0 op_sel:[1,0,0]
	s_branch .Lic2_s24

.Lic2_s24:
	v_pk_fma_f16 v17, v63, v17, v19 op_sel_hi:[0,1,1]
	v_pk_fma_f16 v19, v63, v23, v20 op_sel_hi:[0,1,1]
	v_pk_fma_f16 v16, v63, v16, v18 op_sel_hi:[0,1,1]
	v_pk_fma_f16 v18, v63, v21, v22 op_sel_hi:[0,1,1]
	s_waitcnt vmcnt(3)
	v_cvt_scalef32_pk_f16_fp8 v20, v14, 1.0
	v_cvt_scalef32_pk_f16_fp8 v14, v14, 1.0 op_sel:[1,0,0]
	v_cvt_scalef32_pk_f16_fp8 v21, v15, 1.0
	v_cvt_scalef32_pk_f16_fp8 v15, v15, 1.0 op_sel:[1,0,0]
	v_pk_fma_f16 v18, v63, v20, v18 op_sel_hi:[0,1,1]
	v_pk_fma_f16 v14, v63, v14, v16 op_sel_hi:[0,1,1]
	v_pk_fma_f16 v16, v63, v21, v19 op_sel_hi:[0,1,1]
	v_pk_fma_f16 v15, v63, v15, v17 op_sel_hi:[0,1,1]
	s_waitcnt vmcnt(2)
	s_branch .Lic2_s25

.Lic2_s25:
	v_cvt_scalef32_pk_f16_fp8 v17, v12, 1.0
	v_cvt_scalef32_pk_f16_fp8 v12, v12, 1.0 op_sel:[1,0,0]
	v_cvt_scalef32_pk_f16_fp8 v19, v13, 1.0
	v_cvt_scalef32_pk_f16_fp8 v13, v13, 1.0 op_sel:[1,0,0]
	v_pk_fma_f16 v13, v63, v13, v15 op_sel_hi:[0,1,1]
	v_pk_fma_f16 v15, v63, v19, v16 op_sel_hi:[0,1,1]
	v_pk_fma_f16 v12, v63, v12, v14 op_sel_hi:[0,1,1]
	v_pk_fma_f16 v14, v63, v17, v18 op_sel_hi:[0,1,1]
	s_waitcnt vmcnt(1)
	v_cvt_scalef32_pk_f16_fp8 v16, v10, 1.0
	v_cvt_scalef32_pk_f16_fp8 v10, v10, 1.0 op_sel:[1,0,0]
	v_cvt_scalef32_pk_f16_fp8 v17, v11, 1.0
	v_cvt_scalef32_pk_f16_fp8 v11, v11, 1.0 op_sel:[1,0,0]
	v_pk_fma_f16 v16, v63, v16, v14 op_sel_hi:[0,1,1]
	s_branch .Lic2_s26

.Lic2_s26:
	v_pk_fma_f16 v10, v63, v10, v12 op_sel_hi:[0,1,1]
	v_pk_fma_f16 v12, v63, v17, v15 op_sel_hi:[0,1,1]
	v_pk_fma_f16 v11, v63, v11, v13 op_sel_hi:[0,1,1]
	s_waitcnt vmcnt(0)
	v_cvt_scalef32_pk_f16_fp8 v17, v8, 1.0
	v_cvt_scalef32_pk_f16_fp8 v8, v8, 1.0 op_sel:[1,0,0]
	v_cvt_scalef32_pk_f16_fp8 v13, v9, 1.0
	v_cvt_scalef32_pk_f16_fp8 v9, v9, 1.0 op_sel:[1,0,0]
	v_pk_fma_f16 v15, v63, v9, v11 op_sel_hi:[0,1,1]
	v_pk_fma_f16 v14, v63, v13, v12 op_sel_hi:[0,1,1]
	v_pk_fma_f16 v13, v63, v8, v10 op_sel_hi:[0,1,1]
	s_andn2_b64 vcc, exec, s[36:37]
	v_pk_fma_f16 v12, v63, v17, v16 op_sel_hi:[0,1,1]
	s_cbranch_vccnz .LBB5_50
	v_cvt_scalef32_pk_f16_fp8 v8, v34, 1.0
	s_branch .Lic2_s27

.Lic2_s27:
	v_cvt_scalef32_pk_f16_fp8 v9, v34, 1.0 op_sel:[1,0,0]
	v_cvt_scalef32_pk_f16_fp8 v10, v35, 1.0
	v_cvt_scalef32_pk_f16_fp8 v11, v35, 1.0 op_sel:[1,0,0]
	v_pk_fma_f16 v8, v60, v8, v12
	v_pk_fma_f16 v9, v60, v9, v13
	v_pk_fma_f16 v10, v60, v10, v14
	v_pk_fma_f16 v11, v60, v11, v15
	v_cvt_scalef32_pk_f16_fp8 v12, v38, 1.0
	v_cvt_scalef32_pk_f16_fp8 v13, v38, 1.0 op_sel:[1,0,0]
	v_cvt_scalef32_pk_f16_fp8 v14, v39, 1.0
	v_cvt_scalef32_pk_f16_fp8 v15, v39, 1.0 op_sel:[1,0,0]
	v_pk_fma_f16 v15, v60, v15, v11
	v_pk_fma_f16 v14, v60, v14, v10
	v_pk_fma_f16 v13, v60, v13, v9
	s_branch .Lic2_s28

.Lic2_s28:
	v_pk_fma_f16 v12, v60, v12, v8
.LBB5_50:
	s_andn2_b64 vcc, exec, s[34:35]
	s_cbranch_vccnz .LBB5_52
	v_cvt_scalef32_pk_f16_fp8 v8, v36, 1.0
	v_cvt_scalef32_pk_f16_fp8 v9, v36, 1.0 op_sel:[1,0,0]
	v_cvt_scalef32_pk_f16_fp8 v10, v37, 1.0
	v_cvt_scalef32_pk_f16_fp8 v11, v37, 1.0 op_sel:[1,0,0]
	v_pk_fma_f16 v8, v60, v8, v12
	v_pk_fma_f16 v9, v60, v9, v13
	v_pk_fma_f16 v10, v60, v10, v14
	v_pk_fma_f16 v11, v60, v11, v15
	v_cvt_scalef32_pk_f16_fp8 v12, v42, 1.0
	v_cvt_scalef32_pk_f16_fp8 v13, v42, 1.0 op_sel:[1,0,0]
	v_cvt_scalef32_pk_f16_fp8 v14, v43, 1.0
	s_branch .Lic2_s29

.Lic2_s29:
	v_cvt_scalef32_pk_f16_fp8 v15, v43, 1.0 op_sel:[1,0,0]
	v_pk_fma_f16 v15, v60, v15, v11
	v_pk_fma_f16 v14, v60, v14, v10
	v_pk_fma_f16 v13, v60, v13, v9
	v_pk_fma_f16 v12, v60, v12, v8
.LBB5_52:
	s_andn2_b64 vcc, exec, s[10:11]
	s_cbranch_vccnz .LBB5_54
	v_cvt_scalef32_pk_f16_fp8 v8, v40, 1.0
	v_cvt_scalef32_pk_f16_fp8 v9, v40, 1.0 op_sel:[1,0,0]
	v_cvt_scalef32_pk_f16_fp8 v10, v41, 1.0
	v_cvt_scalef32_pk_f16_fp8 v11, v41, 1.0 op_sel:[1,0,0]
	v_pk_fma_f16 v8, v60, v8, v12
	v_pk_fma_f16 v9, v60, v9, v13
	v_pk_fma_f16 v10, v60, v10, v14
	s_branch .Lic2_s30

.Lic2_s30:
	v_pk_fma_f16 v11, v60, v11, v15
	v_cvt_scalef32_pk_f16_fp8 v12, v46, 1.0
	v_cvt_scalef32_pk_f16_fp8 v13, v46, 1.0 op_sel:[1,0,0]
	v_cvt_scalef32_pk_f16_fp8 v14, v47, 1.0
	v_cvt_scalef32_pk_f16_fp8 v15, v47, 1.0 op_sel:[1,0,0]
	v_pk_fma_f16 v15, v60, v15, v11
	v_pk_fma_f16 v14, v60, v14, v10
	v_pk_fma_f16 v13, v60, v13, v9
	v_pk_fma_f16 v12, v60, v12, v8
.LBB5_54:
	s_andn2_b64 vcc, exec, s[8:9]
	s_cbranch_vccnz .LBB5_56
	v_cvt_scalef32_pk_f16_fp8 v8, v44, 1.0
	v_cvt_scalef32_pk_f16_fp8 v9, v44, 1.0 op_sel:[1,0,0]
	v_cvt_scalef32_pk_f16_fp8 v10, v45, 1.0
	s_branch .Lic2_s31

.Lic2_s31:
	v_cvt_scalef32_pk_f16_fp8 v11, v45, 1.0 op_sel:[1,0,0]
	v_pk_fma_f16 v8, v60, v8, v12
	v_pk_fma_f16 v9, v60, v9, v13
	v_pk_fma_f16 v10, v60, v10, v14
	v_pk_fma_f16 v11, v60, v11, v15
	v_cvt_scalef32_pk_f16_fp8 v12, v48, 1.0
	v_cvt_scalef32_pk_f16_fp8 v13, v48, 1.0 op_sel:[1,0,0]
	v_cvt_scalef32_pk_f16_fp8 v14, v49, 1.0
	v_cvt_scalef32_pk_f16_fp8 v15, v49, 1.0 op_sel:[1,0,0]
	v_pk_fma_f16 v15, v60, v15, v11
	v_pk_fma_f16 v14, v60, v14, v10
	v_pk_fma_f16 v13, v60, v13, v9
	v_pk_fma_f16 v12, v60, v12, v8
.LBB5_56:
	v_add_u32_e32 v4, v75, v4
	s_branch .Lic2_s32

.Lic2_s32:
	s_mov_b32 s8, 24
	s_branch .LBB5_58
.LBB5_57:
	s_waitcnt lgkmcnt(0)
	s_or_b64 exec, exec, s[6:7]
	s_nop 1
	v_add_u32_dpp v13, v12, v81 row_newbcast:0 row_mask:0xf bank_mask:0x3
	v_add_u32_dpp v13, v12, v81 row_newbcast:8 row_mask:0xf bank_mask:0xc
	v_add_u32_dpp v20, v12, v81 row_newbcast:3 row_mask:0xf bank_mask:0x3
	v_add_u32_dpp v20, v12, v81 row_newbcast:11 row_mask:0xf bank_mask:0xc
	global_load_dwordx2 v[14:15], v13, s[30:31]
	v_add_u32_dpp v24, v12, v81 row_newbcast:5 row_mask:0xf bank_mask:0x3
	v_add_u32_dpp v24, v12, v81 row_newbcast:13 row_mask:0xf bank_mask:0xc
	global_load_dwordx2 v[20:21], v20, s[30:31]
	v_add_u32_dpp v26, v12, v81 row_newbcast:7 row_mask:0xf bank_mask:0x3
	s_branch .Lic2_s33

.Lic2_s33:
	v_add_u32_dpp v26, v12, v81 row_newbcast:15 row_mask:0xf bank_mask:0xc
	global_load_dwordx2 v[24:25], v24, s[30:31]
	v_add_u32_dpp v16, v12, v81 row_newbcast:1 row_mask:0xf bank_mask:0x3
	v_add_u32_dpp v16, v12, v81 row_newbcast:9 row_mask:0xf bank_mask:0xc
	global_load_dwordx2 v[16:17], v16, s[30:31]
	v_add_u32_dpp v13, v12, v81 row_newbcast:2 row_mask:0xf bank_mask:0x3
	v_add_u32_dpp v13, v12, v81 row_newbcast:10 row_mask:0xf bank_mask:0xc
	global_load_dwordx2 v[18:19], v13, s[30:31]
	global_load_dwordx2 v[26:27], v26, s[30:31]
	s_add_i32 s8, s8, 8
	v_add_u32_dpp v13, v12, v81 row_newbcast:4 row_mask:0xf bank_mask:0x3
	v_add_u32_dpp v13, v12, v81 row_newbcast:12 row_mask:0xf bank_mask:0xc
	global_load_dwordx2 v[22:23], v13, s[30:31]
	v_mov_b32_dpp v13, v12 row_newbcast:6 row_mask:0xf bank_mask:0x3
	s_branch .Lic2_s34

.Lic2_s34:
	v_mov_b32_dpp v13, v12 row_newbcast:14 row_mask:0xf bank_mask:0xc
	v_add_u32_e32 v12, v13, v81
	global_load_dwordx2 v[12:13], v12, s[30:31]
	s_waitcnt vmcnt(7)
	v_cvt_scalef32_pk_f16_fp8 v28, v14, 1.0
	v_cvt_scalef32_pk_f16_fp8 v14, v14, 1.0 op_sel:[1,0,0]
	v_cvt_scalef32_pk_f16_fp8 v29, v15, 1.0
	v_cvt_scalef32_pk_f16_fp8 v15, v15, 1.0 op_sel:[1,0,0]
	v_pk_fma_f16 v28, v60, v28, v8
	v_pk_fma_f16 v14, v60, v14, v9
	v_pk_fma_f16 v29, v60, v29, v10
	s_waitcnt vmcnt(4)
	v_cvt_scalef32_pk_f16_fp8 v30, v16, 1.0
	v_cvt_scalef32_pk_f16_fp8 v16, v16, 1.0 op_sel:[1,0,0]
	s_branch .Lic2_s35

.Lic2_s35:
	v_cvt_scalef32_pk_f16_fp8 v31, v17, 1.0
	v_cvt_scalef32_pk_f16_fp8 v17, v17, 1.0 op_sel:[1,0,0]
	v_pk_fma_f16 v15, v60, v15, v11
	s_waitcnt vmcnt(3)
	v_cvt_scalef32_pk_f16_fp8 v50, v18, 1.0
	v_cvt_scalef32_pk_f16_fp8 v18, v18, 1.0 op_sel:[1,0,0]
	v_cvt_scalef32_pk_f16_fp8 v51, v19, 1.0
	v_cvt_scalef32_pk_f16_fp8 v19, v19, 1.0 op_sel:[1,0,0]
	v_pk_fma_f16 v15, v60, v17, v15
	v_pk_fma_f16 v17, v60, v31, v29
	v_pk_fma_f16 v14, v60, v16, v14
	v_pk_fma_f16 v16, v60, v30, v28
	v_cvt_scalef32_pk_f16_fp8 v52, v20, 1.0
	v_cvt_scalef32_pk_f16_fp8 v20, v20, 1.0 op_sel:[1,0,0]
	s_branch .Lic2_s36

.Lic2_s36:
	v_cvt_scalef32_pk_f16_fp8 v53, v21, 1.0
	v_cvt_scalef32_pk_f16_fp8 v21, v21, 1.0 op_sel:[1,0,0]
	v_pk_fma_f16 v16, v60, v50, v16
	v_pk_fma_f16 v14, v60, v18, v14
	v_pk_fma_f16 v17, v60, v51, v17
	v_pk_fma_f16 v15, v60, v19, v15
	s_waitcnt vmcnt(1)
	v_cvt_scalef32_pk_f16_fp8 v54, v22, 1.0
	v_cvt_scalef32_pk_f16_fp8 v22, v22, 1.0 op_sel:[1,0,0]
	v_cvt_scalef32_pk_f16_fp8 v55, v23, 1.0
	v_cvt_scalef32_pk_f16_fp8 v23, v23, 1.0 op_sel:[1,0,0]
	v_pk_fma_f16 v15, v60, v21, v15
	v_pk_fma_f16 v17, v60, v53, v17
	v_pk_fma_f16 v14, v60, v20, v14
	s_branch .Lic2_s37

.Lic2_s37:
	v_pk_fma_f16 v16, v60, v52, v16
	v_cvt_scalef32_pk_f16_fp8 v56, v24, 1.0
	v_cvt_scalef32_pk_f16_fp8 v24, v24, 1.0 op_sel:[1,0,0]
	v_cvt_scalef32_pk_f16_fp8 v57, v25, 1.0
	v_cvt_scalef32_pk_f16_fp8 v25, v25, 1.0 op_sel:[1,0,0]
	v_pk_fma_f16 v16, v60, v54, v16
	v_pk_fma_f16 v14, v60, v22, v14
	v_pk_fma_f16 v17, v60, v55, v17
	v_pk_fma_f16 v15, v60, v23, v15
	s_waitcnt vmcnt(0)
	v_cvt_scalef32_pk_f16_fp8 v61, v12, 1.0
	v_cvt_scalef32_pk_f16_fp8 v12, v12, 1.0 op_sel:[1,0,0]
	v_cvt_scalef32_pk_f16_fp8 v63, v13, 1.0
	v_cvt_scalef32_pk_f16_fp8 v13, v13, 1.0 op_sel:[1,0,0]
	s_branch .Lic2_s38

.Lic2_s38:
	v_pk_fma_f16 v15, v60, v25, v15
	v_pk_fma_f16 v17, v60, v57, v17
	v_pk_fma_f16 v14, v60, v24, v14
	v_pk_fma_f16 v16, v60, v56, v16
	v_cvt_scalef32_pk_f16_fp8 v64, v26, 1.0
	v_cvt_scalef32_pk_f16_fp8 v26, v26, 1.0 op_sel:[1,0,0]
	v_cvt_scalef32_pk_f16_fp8 v65, v27, 1.0
	v_cvt_scalef32_pk_f16_fp8 v27, v27, 1.0 op_sel:[1,0,0]
	v_pk_fma_f16 v16, v60, v61, v16
	v_pk_fma_f16 v12, v60, v12, v14
	v_pk_fma_f16 v14, v60, v63, v17
	v_pk_fma_f16 v13, v60, v13, v15
	v_pk_fma_f16 v14, v60, v65, v14
	v_pk_fma_f16 v15, v60, v27, v13
	s_branch .Lic2_s39

.Lic2_s39:
	v_pk_fma_f16 v13, v60, v26, v12
	v_pk_fma_f16 v12, v60, v64, v16
.LBB5_58:
	s_waitcnt lgkmcnt(0)
	s_nop 0
	v_mov_b64_e32 v[8:9], v[12:13]
	v_mov_b64_e32 v[10:11], v[14:15]
	v_cmp_lt_i32_e32 vcc, s8, v58
	s_cbranch_vccz .LBB5_61
	v_add_u32_e32 v12, s8, v75
	v_cmp_lt_i32_e32 vcc, v12, v58
	v_mov_b32_e32 v12, 0x61a800
	s_and_saveexec_b64 s[6:7], vcc
	s_cbranch_execz .LBB5_57
	v_add_u32_e32 v12, s8, v4
	s_branch .Lic2_s40

.Lic2_s40:
	v_ashrrev_i32_e32 v13, 31, v12
	v_lshl_add_u64 v[12:13], v[12:13], 2, s[26:27]
	global_load_dword v12, v[12:13], off
	s_waitcnt vmcnt(0)
	v_lshlrev_b32_e32 v12, 6, v12
	v_and_b32_e32 v12, 0x7fffc0, v12
	s_branch .LBB5_57
.LBB5_61:
	s_cbranch_execz .LBB5_58
	ds_write_b128 v82, v[8:11]
	ds_read_b128 v[8:11], v83
	ds_read_b128 v[12:15], v80
	ds_read_b128 v[16:19], v83 offset:8704
	ds_read_b128 v[20:23], v83 offset:17408
	ds_read_b128 v[24:27], v83 offset:26112
	s_branch .Lic2_s41

.Lic2_s41:
	s_waitcnt lgkmcnt(3)
	v_mfma_f32_16x16x32_f16 v[8:11], v[8:11], v[12:15], 0
	s_waitcnt lgkmcnt(2)
	v_mfma_f32_16x16x32_f16 v[16:19], v[16:19], v[12:15], 0
	s_waitcnt lgkmcnt(1)
	v_mfma_f32_16x16x32_f16 v[20:23], v[20:23], v[12:15], 0
	s_waitcnt lgkmcnt(0)
	v_mfma_f32_16x16x32_f16 v[90:93], v[24:27], v[12:15], 0
	ds_read_b128 v[12:15], v83 offset:64
	ds_read_b128 v[94:97], v80 offset:64
	ds_read_b128 v[24:27], v83 offset:8768
	ds_read_b128 v[98:101], v83 offset:17472
	s_waitcnt lgkmcnt(2)
	v_mfma_f32_16x16x32_f16 v[8:11], v[12:15], v[94:97], v[8:11]
	s_branch .Lic2_s42

.Lic2_s42:
	v_add_u32_dpp v4, v59, v81 row_newbcast:0 row_mask:0xf bank_mask:0x3
	v_add_u32_dpp v4, v59, v81 row_newbcast:8 row_mask:0xf bank_mask:0xc
	s_waitcnt lgkmcnt(1)
	v_mfma_f32_16x16x32_f16 v[12:15], v[24:27], v[94:97], v[16:19]
	v_mov_b32_dpp v24, v59 row_newbcast:5 row_mask:0xf bank_mask:0x3
	v_mov_b32_dpp v24, v59 row_newbcast:13 row_mask:0xf bank_mask:0xc
	v_mov_b32_dpp v25, v59 row_newbcast:6 row_mask:0xf bank_mask:0x3
	v_mov_b32_dpp v25, v59 row_newbcast:14 row_mask:0xf bank_mask:0xc
	v_mov_b32_dpp v26, v59 row_newbcast:7 row_mask:0xf bank_mask:0x3
	v_mov_b32_dpp v26, v59 row_newbcast:15 row_mask:0xf bank_mask:0xc
	v_mov_b32_dpp v19, v59 row_newbcast:4 row_mask:0xf bank_mask:0x3
	v_mov_b32_dpp v19, v59 row_newbcast:12 row_mask:0xf bank_mask:0xc
	v_add_u32_dpp v16, v59, v81 row_newbcast:1 row_mask:0xf bank_mask:0x3
	v_add_u32_dpp v16, v59, v81 row_newbcast:9 row_mask:0xf bank_mask:0xc
	s_branch .Lic2_s43

.Lic2_s43:
	v_add_u32_dpp v17, v59, v81 row_newbcast:2 row_mask:0xf bank_mask:0x3
	v_add_u32_dpp v17, v59, v81 row_newbcast:10 row_mask:0xf bank_mask:0xc
	v_add_u32_dpp v18, v59, v81 row_newbcast:3 row_mask:0xf bank_mask:0x3
	v_add_u32_dpp v18, v59, v81 row_newbcast:11 row_mask:0xf bank_mask:0xc
	global_load_dwordx2 v[72:73], v4, s[30:31]
	global_load_dwordx2 v[68:69], v16, s[30:31]
	global_load_dwordx2 v[64:65], v17, s[30:31]
	global_load_dwordx2 v[58:59], v18, s[30:31]
	v_add_u32_e32 v4, v19, v81
	v_add_u32_e32 v16, v24, v81
	v_add_u32_e32 v17, v25, v81
	v_add_u32_e32 v18, v26, v81
	global_load_dwordx2 v[70:71], v4, s[30:31]
	global_load_dwordx2 v[66:67], v16, s[30:31]
	s_branch .Lic2_s44

.Lic2_s44:
	global_load_dwordx2 v[60:61], v17, s[30:31]
	global_load_dwordx2 v[54:55], v18, s[30:31]
	v_add_u32_dpp v4, v62, v81 row_newbcast:0 row_mask:0xf bank_mask:0x3
	v_add_u32_dpp v4, v62, v81 row_newbcast:8 row_mask:0xf bank_mask:0xc
	v_mov_b32_dpp v19, v62 row_newbcast:4 row_mask:0xf bank_mask:0x3
	v_mov_b32_dpp v19, v62 row_newbcast:12 row_mask:0xf bank_mask:0xc
	v_add_u32_dpp v16, v62, v81 row_newbcast:1 row_mask:0xf bank_mask:0x3
	v_add_u32_dpp v16, v62, v81 row_newbcast:9 row_mask:0xf bank_mask:0xc
	v_add_u32_dpp v17, v62, v81 row_newbcast:2 row_mask:0xf bank_mask:0x3
	v_add_u32_dpp v17, v62, v81 row_newbcast:10 row_mask:0xf bank_mask:0xc
	v_add_u32_dpp v18, v62, v81 row_newbcast:3 row_mask:0xf bank_mask:0x3
	v_add_u32_dpp v18, v62, v81 row_newbcast:11 row_mask:0xf bank_mask:0xc
	v_mov_b32_dpp v24, v62 row_newbcast:5 row_mask:0xf bank_mask:0x3
	v_mov_b32_dpp v24, v62 row_newbcast:13 row_mask:0xf bank_mask:0xc
	s_branch .Lic2_s45

.Lic2_s45:
	v_mov_b32_dpp v25, v62 row_newbcast:6 row_mask:0xf bank_mask:0x3
	v_mov_b32_dpp v25, v62 row_newbcast:14 row_mask:0xf bank_mask:0xc
	v_mov_b32_dpp v26, v62 row_newbcast:7 row_mask:0xf bank_mask:0x3
	v_mov_b32_dpp v26, v62 row_newbcast:15 row_mask:0xf bank_mask:0xc
	global_load_dwordx2 v[62:63], v4, s[30:31]
	global_load_dwordx2 v[56:57], v16, s[30:31]
	global_load_dwordx2 v[52:53], v17, s[30:31]
	global_load_dwordx2 v[50:51], v18, s[30:31]
	v_add_u32_e32 v4, v19, v81
	v_add_u32_e32 v16, v24, v81
	v_add_u32_e32 v17, v25, v81
	v_add_u32_e32 v18, v26, v81
	global_load_dwordx2 v[30:31], v4, s[30:31]
	global_load_dwordx2 v[28:29], v16, s[30:31]
	s_branch .Lic2_s46

.Lic2_s46:
	global_load_dwordx2 v[26:27], v17, s[30:31]
	global_load_dwordx2 v[24:25], v18, s[30:31]
	s_waitcnt lgkmcnt(0)
	v_mfma_f32_16x16x32_f16 v[16:19], v[98:101], v[94:97], v[20:23]
	v_cmp_lt_i32_e32 vcc, 16, v87
	s_cmp_lg_u64 vcc, 0
	s_cselect_b64 s[36:37], -1, 0
	ds_read_b128 v[20:23], v83 offset:26176
	s_waitcnt lgkmcnt(0)
	v_mfma_f32_16x16x32_f16 v[20:23], v[20:23], v[94:97], v[90:93]
	v_cmp_lt_i32_e64 s[10:11], 18, v87
	v_cmp_lt_i32_e64 s[8:9], 20, v87
	v_cmp_lt_i32_e64 s[6:7], 22, v87
	s_cbranch_vccz .LBB5_64
	v_add_u32_dpp v4, v89, v81 row_newbcast:0 row_mask:0xf bank_mask:0x3
	s_branch .Lic2_s47

.Lic2_s47:
	v_add_u32_dpp v4, v89, v81 row_newbcast:8 row_mask:0xf bank_mask:0xc
	v_add_u32_dpp v38, v89, v81 row_newbcast:1 row_mask:0xf bank_mask:0x3
	v_add_u32_dpp v38, v89, v81 row_newbcast:9 row_mask:0xf bank_mask:0xc
	global_load_dwordx2 v[34:35], v4, s[30:31]
	s_nop 0
	global_load_dwordx2 v[38:39], v38, s[30:31]
.LBB5_64:
	s_cmp_lg_u64 s[10:11], 0
	s_cselect_b64 s[34:35], -1, 0
	s_cmp_eq_u64 s[10:11], 0
	s_cbranch_scc1 .LBB5_66
	v_add_u32_dpp v4, v89, v81 row_newbcast:2 row_mask:0xf bank_mask:0x3
	v_add_u32_dpp v4, v89, v81 row_newbcast:10 row_mask:0xf bank_mask:0xc
	v_add_u32_dpp v42, v89, v81 row_newbcast:3 row_mask:0xf bank_mask:0x3
	v_add_u32_dpp v42, v89, v81 row_newbcast:11 row_mask:0xf bank_mask:0xc
	s_branch .Lic2_s48

.Lic2_s48:
	global_load_dwordx2 v[36:37], v4, s[30:31]
	s_nop 0
	global_load_dwordx2 v[42:43], v42, s[30:31]

.LBB5_68:
	s_cmp_lg_u64 s[6:7], 0
	s_branch .Lic2_s49

.Lic2_s49:
	s_cselect_b64 s[8:9], -1, 0
	s_cmp_eq_u64 s[6:7], 0
	s_cbranch_scc1 .LBB5_70
	v_add_u32_dpp v4, v89, v81 row_newbcast:6 row_mask:0xf bank_mask:0x3
	v_add_u32_dpp v4, v89, v81 row_newbcast:14 row_mask:0xf bank_mask:0xc
	v_add_u32_dpp v48, v89, v81 row_newbcast:7 row_mask:0xf bank_mask:0x3
	v_add_u32_dpp v48, v89, v81 row_newbcast:15 row_mask:0xf bank_mask:0xc
	global_load_dwordx2 v[44:45], v4, s[30:31]
	s_nop 0
	global_load_dwordx2 v[48:49], v48, s[30:31]
.LBB5_70:
	v_cvt_f32_i32_e32 v4, v87
	s_waitcnt vmcnt(15)
	v_cvt_scalef32_pk_f16_fp8 v91, v72, 1.0
	v_cvt_scalef32_pk_f16_fp8 v72, v72, 1.0 op_sel:[1,0,0]
	s_branch .Lic2_s50

.Lic2_s50:
	v_max_f32_e32 v4, 1.0, v4
	v_div_scale_f32 v89, s[6:7], v4, v4, 1.0
	v_rcp_f32_e32 v90, v89
	v_div_scale_f32 v92, vcc, 1.0, v4, 1.0
	v_fma_f32 v93, -v89, v90, 1.0
	v_fmac_f32_e32 v90, v93, v90
	v_mul_f32_e32 v93, v92, v90
	v_fma_f32 v94, -v89, v93, v92
	v_fmac_f32_e32 v93, v94, v90
	v_fma_f32 v89, -v89, v93, v92
	v_div_fmas_f32 v89, v89, v90, v93
	v_div_fixup_f32 v4, v89, v4, 1.0
	v_mul_f32_e32 v89, 0x3c800000, v4
	v_fma_mixlo_f16 v90, v4, s29, 0
	s_branch .Lic2_s51

.Lic2_s51:
	v_cvt_pk_f16_f32 v4, v89, v89
	v_cvt_scalef32_pk_f16_fp8 v89, v73, 1.0
	v_cvt_scalef32_pk_f16_fp8 v73, v73, 1.0 op_sel:[1,0,0]
	v_pk_fma_f16 v91, v90, v91, 0 op_sel_hi:[0,1,1]
	v_pk_fma_f16 v72, v90, v72, 0 op_sel_hi:[0,1,1]
	v_pk_fma_f16 v89, v90, v89, 0 op_sel_hi:[0,1,1]
	v_pk_fma_f16 v73, v90, v73, 0 op_sel_hi:[0,1,1]
	s_waitcnt vmcnt(14)
	v_cvt_scalef32_pk_f16_fp8 v92, v68, 1.0
	v_cvt_scalef32_pk_f16_fp8 v68, v68, 1.0 op_sel:[1,0,0]
	v_cvt_scalef32_pk_f16_fp8 v93, v69, 1.0
	v_cvt_scalef32_pk_f16_fp8 v69, v69, 1.0 op_sel:[1,0,0]
	v_pk_fma_f16 v69, v90, v69, v73 op_sel_hi:[0,1,1]
	v_pk_fma_f16 v73, v90, v93, v89 op_sel_hi:[0,1,1]
	s_branch .Lic2_s52

.Lic2_s52:
	v_pk_fma_f16 v68, v90, v68, v72 op_sel_hi:[0,1,1]
	v_pk_fma_f16 v72, v90, v92, v91 op_sel_hi:[0,1,1]
	s_waitcnt vmcnt(13)
	v_cvt_scalef32_pk_f16_fp8 v89, v64, 1.0
	v_cvt_scalef32_pk_f16_fp8 v64, v64, 1.0 op_sel:[1,0,0]
	v_cvt_scalef32_pk_f16_fp8 v91, v65, 1.0
	v_cvt_scalef32_pk_f16_fp8 v65, v65, 1.0 op_sel:[1,0,0]
	v_pk_fma_f16 v72, v90, v89, v72 op_sel_hi:[0,1,1]
	v_pk_fma_f16 v64, v90, v64, v68 op_sel_hi:[0,1,1]
	v_pk_fma_f16 v68, v90, v91, v73 op_sel_hi:[0,1,1]
	v_pk_fma_f16 v65, v90, v65, v69 op_sel_hi:[0,1,1]
	s_waitcnt vmcnt(12)
	v_cvt_scalef32_pk_f16_fp8 v69, v58, 1.0
	v_cvt_scalef32_pk_f16_fp8 v58, v58, 1.0 op_sel:[1,0,0]
	s_branch .Lic2_s53

.Lic2_s53:
	v_cvt_scalef32_pk_f16_fp8 v73, v59, 1.0
	v_cvt_scalef32_pk_f16_fp8 v59, v59, 1.0 op_sel:[1,0,0]
	v_pk_fma_f16 v59, v90, v59, v65 op_sel_hi:[0,1,1]
	v_pk_fma_f16 v65, v90, v73, v68 op_sel_hi:[0,1,1]
	v_pk_fma_f16 v58, v90, v58, v64 op_sel_hi:[0,1,1]
	v_pk_fma_f16 v64, v90, v69, v72 op_sel_hi:[0,1,1]
	s_waitcnt vmcnt(11)
	v_cvt_scalef32_pk_f16_fp8 v68, v70, 1.0
	v_cvt_scalef32_pk_f16_fp8 v69, v70, 1.0 op_sel:[1,0,0]
	v_cvt_scalef32_pk_f16_fp8 v70, v71, 1.0
	v_cvt_scalef32_pk_f16_fp8 v71, v71, 1.0 op_sel:[1,0,0]
	v_pk_fma_f16 v64, v90, v68, v64 op_sel_hi:[0,1,1]
	v_pk_fma_f16 v58, v90, v69, v58 op_sel_hi:[0,1,1]
	v_pk_fma_f16 v65, v90, v70, v65 op_sel_hi:[0,1,1]
	s_branch .Lic2_s54

.Lic2_s54:
	v_pk_fma_f16 v59, v90, v71, v59 op_sel_hi:[0,1,1]
	s_waitcnt vmcnt(10)
	v_cvt_scalef32_pk_f16_fp8 v68, v66, 1.0
	v_cvt_scalef32_pk_f16_fp8 v66, v66, 1.0 op_sel:[1,0,0]
	v_cvt_scalef32_pk_f16_fp8 v69, v67, 1.0
	v_cvt_scalef32_pk_f16_fp8 v67, v67, 1.0 op_sel:[1,0,0]
	v_pk_fma_f16 v59, v90, v67, v59 op_sel_hi:[0,1,1]
	v_pk_fma_f16 v65, v90, v69, v65 op_sel_hi:[0,1,1]
	v_pk_fma_f16 v58, v90, v66, v58 op_sel_hi:[0,1,1]
	v_pk_fma_f16 v64, v90, v68, v64 op_sel_hi:[0,1,1]
	s_waitcnt vmcnt(9)
	v_cvt_scalef32_pk_f16_fp8 v66, v60, 1.0
	v_cvt_scalef32_pk_f16_fp8 v60, v60, 1.0 op_sel:[1,0,0]
	v_cvt_scalef32_pk_f16_fp8 v67, v61, 1.0
	s_branch .Lic2_s55

.Lic2_s55:
	v_cvt_scalef32_pk_f16_fp8 v61, v61, 1.0 op_sel:[1,0,0]
	v_pk_fma_f16 v64, v90, v66, v64 op_sel_hi:[0,1,1]
	v_pk_fma_f16 v58, v90, v60, v58 op_sel_hi:[0,1,1]
	v_pk_fma_f16 v60, v90, v67, v65 op_sel_hi:[0,1,1]
	v_pk_fma_f16 v59, v90, v61, v59 op_sel_hi:[0,1,1]
	s_waitcnt vmcnt(8)
	v_cvt_scalef32_pk_f16_fp8 v61, v54, 1.0
	v_cvt_scalef32_pk_f16_fp8 v54, v54, 1.0 op_sel:[1,0,0]
	v_cvt_scalef32_pk_f16_fp8 v65, v55, 1.0
	v_cvt_scalef32_pk_f16_fp8 v55, v55, 1.0 op_sel:[1,0,0]
	v_pk_fma_f16 v55, v90, v55, v59 op_sel_hi:[0,1,1]
	v_pk_fma_f16 v59, v90, v65, v60 op_sel_hi:[0,1,1]
	v_pk_fma_f16 v54, v90, v54, v58 op_sel_hi:[0,1,1]
	v_pk_fma_f16 v58, v90, v61, v64 op_sel_hi:[0,1,1]
	s_branch .Lic2_s56

.Lic2_s56:
	s_waitcnt vmcnt(7)
	v_cvt_scalef32_pk_f16_fp8 v60, v62, 1.0
	v_cvt_scalef32_pk_f16_fp8 v61, v62, 1.0 op_sel:[1,0,0]
	v_cvt_scalef32_pk_f16_fp8 v62, v63, 1.0
	v_cvt_scalef32_pk_f16_fp8 v63, v63, 1.0 op_sel:[1,0,0]
	v_pk_fma_f16 v58, v90, v60, v58 op_sel_hi:[0,1,1]
	v_pk_fma_f16 v54, v90, v61, v54 op_sel_hi:[0,1,1]
	v_pk_fma_f16 v59, v90, v62, v59 op_sel_hi:[0,1,1]
	v_pk_fma_f16 v55, v90, v63, v55 op_sel_hi:[0,1,1]
	s_waitcnt vmcnt(6)
	v_cvt_scalef32_pk_f16_fp8 v60, v56, 1.0
	v_cvt_scalef32_pk_f16_fp8 v56, v56, 1.0 op_sel:[1,0,0]
	v_cvt_scalef32_pk_f16_fp8 v61, v57, 1.0
	v_cvt_scalef32_pk_f16_fp8 v57, v57, 1.0 op_sel:[1,0,0]
	s_branch .Lic2_s57

.Lic2_s57:
	v_pk_fma_f16 v55, v90, v57, v55 op_sel_hi:[0,1,1]
	v_pk_fma_f16 v57, v90, v61, v59 op_sel_hi:[0,1,1]
	v_pk_fma_f16 v54, v90, v56, v54 op_sel_hi:[0,1,1]
	v_pk_fma_f16 v56, v90, v60, v58 op_sel_hi:[0,1,1]
	s_waitcnt vmcnt(5)
	v_cvt_scalef32_pk_f16_fp8 v58, v52, 1.0
	v_cvt_scalef32_pk_f16_fp8 v52, v52, 1.0 op_sel:[1,0,0]
	v_cvt_scalef32_pk_f16_fp8 v59, v53, 1.0
	v_cvt_scalef32_pk_f16_fp8 v53, v53, 1.0 op_sel:[1,0,0]
	v_pk_fma_f16 v56, v90, v58, v56 op_sel_hi:[0,1,1]
	v_pk_fma_f16 v52, v90, v52, v54 op_sel_hi:[0,1,1]
	v_pk_fma_f16 v54, v90, v59, v57 op_sel_hi:[0,1,1]
	v_pk_fma_f16 v53, v90, v53, v55 op_sel_hi:[0,1,1]
	s_waitcnt vmcnt(4)
	s_branch .Lic2_s58

.Lic2_s58:
	v_cvt_scalef32_pk_f16_fp8 v55, v50, 1.0
	v_cvt_scalef32_pk_f16_fp8 v50, v50, 1.0 op_sel:[1,0,0]
	v_cvt_scalef32_pk_f16_fp8 v57, v51, 1.0
	v_cvt_scalef32_pk_f16_fp8 v51, v51, 1.0 op_sel:[1,0,0]
	v_pk_fma_f16 v51, v90, v51, v53 op_sel_hi:[0,1,1]
	v_pk_fma_f16 v53, v90, v57, v54 op_sel_hi:[0,1,1]
	v_pk_fma_f16 v50, v90, v50, v52 op_sel_hi:[0,1,1]
	v_pk_fma_f16 v52, v90, v55, v56 op_sel_hi:[0,1,1]
	s_waitcnt vmcnt(3)
	v_cvt_scalef32_pk_f16_fp8 v54, v30, 1.0
	v_cvt_scalef32_pk_f16_fp8 v30, v30, 1.0 op_sel:[1,0,0]
	v_cvt_scalef32_pk_f16_fp8 v55, v31, 1.0
	v_cvt_scalef32_pk_f16_fp8 v31, v31, 1.0 op_sel:[1,0,0]
	v_pk_fma_f16 v52, v90, v54, v52 op_sel_hi:[0,1,1]
	s_branch .Lic2_s59

.Lic2_s59:
	v_pk_fma_f16 v30, v90, v30, v50 op_sel_hi:[0,1,1]
	v_pk_fma_f16 v50, v90, v55, v53 op_sel_hi:[0,1,1]
	v_pk_fma_f16 v31, v90, v31, v51 op_sel_hi:[0,1,1]
	s_waitcnt vmcnt(2)
	v_cvt_scalef32_pk_f16_fp8 v51, v28, 1.0
	v_cvt_scalef32_pk_f16_fp8 v28, v28, 1.0 op_sel:[1,0,0]
	v_cvt_scalef32_pk_f16_fp8 v53, v29, 1.0
	v_cvt_scalef32_pk_f16_fp8 v29, v29, 1.0 op_sel:[1,0,0]
	v_pk_fma_f16 v29, v90, v29, v31 op_sel_hi:[0,1,1]
	v_pk_fma_f16 v31, v90, v53, v50 op_sel_hi:[0,1,1]
	v_pk_fma_f16 v28, v90, v28, v30 op_sel_hi:[0,1,1]
	v_pk_fma_f16 v30, v90, v51, v52 op_sel_hi:[0,1,1]
	s_waitcnt vmcnt(1)
	v_cvt_scalef32_pk_f16_fp8 v50, v26, 1.0
	s_branch .Lic2_s60

.Lic2_s60:
	v_cvt_scalef32_pk_f16_fp8 v26, v26, 1.0 op_sel:[1,0,0]
	v_cvt_scalef32_pk_f16_fp8 v51, v27, 1.0
	v_cvt_scalef32_pk_f16_fp8 v27, v27, 1.0 op_sel:[1,0,0]
	v_pk_fma_f16 v50, v90, v50, v30 op_sel_hi:[0,1,1]
	v_pk_fma_f16 v26, v90, v26, v28 op_sel_hi:[0,1,1]
	v_pk_fma_f16 v28, v90, v51, v31 op_sel_hi:[0,1,1]
	v_pk_fma_f16 v27, v90, v27, v29 op_sel_hi:[0,1,1]
	s_waitcnt vmcnt(0)
	v_cvt_scalef32_pk_f16_fp8 v51, v24, 1.0
	v_cvt_scalef32_pk_f16_fp8 v24, v24, 1.0 op_sel:[1,0,0]
	v_cvt_scalef32_pk_f16_fp8 v29, v25, 1.0
	v_cvt_scalef32_pk_f16_fp8 v25, v25, 1.0 op_sel:[1,0,0]
	v_pk_fma_f16 v31, v90, v25, v27 op_sel_hi:[0,1,1]
	v_pk_fma_f16 v30, v90, v29, v28 op_sel_hi:[0,1,1]
	s_branch .Lic2_s61

.Lic2_s61:
	v_pk_fma_f16 v29, v90, v24, v26 op_sel_hi:[0,1,1]
	s_andn2_b64 vcc, exec, s[36:37]
	v_pk_fma_f16 v28, v90, v51, v50 op_sel_hi:[0,1,1]
	s_cbranch_vccnz .LBB5_72
	v_cvt_scalef32_pk_f16_fp8 v24, v34, 1.0
	v_cvt_scalef32_pk_f16_fp8 v25, v34, 1.0 op_sel:[1,0,0]
	v_cvt_scalef32_pk_f16_fp8 v26, v35, 1.0
	v_cvt_scalef32_pk_f16_fp8 v27, v35, 1.0 op_sel:[1,0,0]
	v_pk_fma_f16 v24, v4, v24, v28
	v_pk_fma_f16 v25, v4, v25, v29
	v_pk_fma_f16 v26, v4, v26, v30
	v_pk_fma_f16 v27, v4, v27, v31
	v_cvt_scalef32_pk_f16_fp8 v28, v38, 1.0
	v_cvt_scalef32_pk_f16_fp8 v29, v38, 1.0 op_sel:[1,0,0]
	s_branch .Lic2_s62

.Lic2_s62:
	v_cvt_scalef32_pk_f16_fp8 v30, v39, 1.0
	v_cvt_scalef32_pk_f16_fp8 v31, v39, 1.0 op_sel:[1,0,0]
	v_pk_fma_f16 v31, v4, v31, v27
	v_pk_fma_f16 v30, v4, v30, v26
	v_pk_fma_f16 v29, v4, v29, v25
	v_pk_fma_f16 v28, v4, v28, v24
.LBB5_72:
	s_andn2_b64 vcc, exec, s[34:35]
	s_cbranch_vccnz .LBB5_74
	v_cvt_scalef32_pk_f16_fp8 v24, v36, 1.0
	v_cvt_scalef32_pk_f16_fp8 v25, v36, 1.0 op_sel:[1,0,0]
	v_cvt_scalef32_pk_f16_fp8 v26, v37, 1.0
	v_cvt_scalef32_pk_f16_fp8 v27, v37, 1.0 op_sel:[1,0,0]
	v_pk_fma_f16 v24, v4, v24, v28
	v_pk_fma_f16 v25, v4, v25, v29
	s_branch .Lic2_s63

.Lic2_s63:
	v_pk_fma_f16 v26, v4, v26, v30
	v_pk_fma_f16 v27, v4, v27, v31
	v_cvt_scalef32_pk_f16_fp8 v28, v42, 1.0
	v_cvt_scalef32_pk_f16_fp8 v29, v42, 1.0 op_sel:[1,0,0]
	v_cvt_scalef32_pk_f16_fp8 v30, v43, 1.0
	v_cvt_scalef32_pk_f16_fp8 v31, v43, 1.0 op_sel:[1,0,0]
	v_pk_fma_f16 v31, v4, v31, v27
	v_pk_fma_f16 v30, v4, v30, v26
	v_pk_fma_f16 v29, v4, v29, v25
	v_pk_fma_f16 v28, v4, v28, v24
.LBB5_74:
	s_andn2_b64 vcc, exec, s[10:11]
	s_cbranch_vccnz .LBB5_76
	v_cvt_scalef32_pk_f16_fp8 v24, v40, 1.0
	v_cvt_scalef32_pk_f16_fp8 v25, v40, 1.0 op_sel:[1,0,0]
	s_branch .Lic2_s64

.Lic2_s64:
	v_cvt_scalef32_pk_f16_fp8 v26, v41, 1.0
	v_cvt_scalef32_pk_f16_fp8 v27, v41, 1.0 op_sel:[1,0,0]
	v_pk_fma_f16 v24, v4, v24, v28
	v_pk_fma_f16 v25, v4, v25, v29
	v_pk_fma_f16 v26, v4, v26, v30
	v_pk_fma_f16 v27, v4, v27, v31
	v_cvt_scalef32_pk_f16_fp8 v28, v46, 1.0
	v_cvt_scalef32_pk_f16_fp8 v29, v46, 1.0 op_sel:[1,0,0]
	v_cvt_scalef32_pk_f16_fp8 v30, v47, 1.0
	v_cvt_scalef32_pk_f16_fp8 v31, v47, 1.0 op_sel:[1,0,0]
	v_pk_fma_f16 v31, v4, v31, v27
	v_pk_fma_f16 v30, v4, v30, v26
	v_pk_fma_f16 v29, v4, v29, v25
	v_pk_fma_f16 v28, v4, v28, v24
.LBB5_76:
	s_andn2_b64 vcc, exec, s[8:9]
	s_branch .Lic2_s65

.Lic2_s65:
	s_cbranch_vccnz .LBB5_78
	v_cvt_scalef32_pk_f16_fp8 v24, v44, 1.0
	v_cvt_scalef32_pk_f16_fp8 v25, v44, 1.0 op_sel:[1,0,0]
	v_cvt_scalef32_pk_f16_fp8 v26, v45, 1.0
	v_cvt_scalef32_pk_f16_fp8 v27, v45, 1.0 op_sel:[1,0,0]
	v_pk_fma_f16 v24, v4, v24, v28
	v_pk_fma_f16 v25, v4, v25, v29
	v_pk_fma_f16 v26, v4, v26, v30
	v_pk_fma_f16 v27, v4, v27, v31
	v_cvt_scalef32_pk_f16_fp8 v28, v48, 1.0
	v_cvt_scalef32_pk_f16_fp8 v29, v48, 1.0 op_sel:[1,0,0]
	v_cvt_scalef32_pk_f16_fp8 v30, v49, 1.0
	v_cvt_scalef32_pk_f16_fp8 v31, v49, 1.0 op_sel:[1,0,0]
	v_pk_fma_f16 v31, v4, v31, v27
	s_branch .Lic2_s66

.Lic2_s66:
	v_pk_fma_f16 v30, v4, v30, v26
	v_pk_fma_f16 v29, v4, v29, v25
	v_pk_fma_f16 v28, v4, v28, v24

.LBB5_79:
	s_waitcnt lgkmcnt(0)
	s_or_b64 exec, exec, s[6:7]
	s_nop 1
	v_add_u32_dpp v29, v28, v81 row_newbcast:0 row_mask:0xf bank_mask:0x3
	v_add_u32_dpp v29, v28, v81 row_newbcast:8 row_mask:0xf bank_mask:0xc
	v_add_u32_dpp v54, v28, v81 row_newbcast:3 row_mask:0xf bank_mask:0x3
	v_add_u32_dpp v54, v28, v81 row_newbcast:11 row_mask:0xf bank_mask:0xc
	global_load_dwordx2 v[30:31], v29, s[30:31]
	s_branch .Lic2_s67

.Lic2_s67:
	v_add_u32_dpp v58, v28, v81 row_newbcast:5 row_mask:0xf bank_mask:0x3
	v_add_u32_dpp v58, v28, v81 row_newbcast:13 row_mask:0xf bank_mask:0xc
	global_load_dwordx2 v[54:55], v54, s[30:31]
	v_add_u32_dpp v60, v28, v81 row_newbcast:7 row_mask:0xf bank_mask:0x3
	v_add_u32_dpp v60, v28, v81 row_newbcast:15 row_mask:0xf bank_mask:0xc
	global_load_dwordx2 v[58:59], v58, s[30:31]
	v_add_u32_dpp v50, v28, v81 row_newbcast:1 row_mask:0xf bank_mask:0x3
	v_add_u32_dpp v50, v28, v81 row_newbcast:9 row_mask:0xf bank_mask:0xc
	global_load_dwordx2 v[50:51], v50, s[30:31]
	v_add_u32_dpp v29, v28, v81 row_newbcast:2 row_mask:0xf bank_mask:0x3
	v_add_u32_dpp v29, v28, v81 row_newbcast:10 row_mask:0xf bank_mask:0xc
	global_load_dwordx2 v[52:53], v29, s[30:31]
	global_load_dwordx2 v[60:61], v60, s[30:31]
	s_add_i32 s8, s8, 8
	v_add_u32_dpp v29, v28, v81 row_newbcast:4 row_mask:0xf bank_mask:0x3
	s_branch .Lic2_s68

.Lic2_s68:
	v_add_u32_dpp v29, v28, v81 row_newbcast:12 row_mask:0xf bank_mask:0xc
	global_load_dwordx2 v[56:57], v29, s[30:31]
	v_mov_b32_dpp v29, v28 row_newbcast:6 row_mask:0xf bank_mask:0x3
	v_mov_b32_dpp v29, v28 row_newbcast:14 row_mask:0xf bank_mask:0xc
	v_add_u32_e32 v28, v29, v81
	global_load_dwordx2 v[28:29], v28, s[30:31]
	s_waitcnt vmcnt(7)
	v_cvt_scalef32_pk_f16_fp8 v62, v30, 1.0
	v_cvt_scalef32_pk_f16_fp8 v30, v30, 1.0 op_sel:[1,0,0]
	v_cvt_scalef32_pk_f16_fp8 v63, v31, 1.0
	v_cvt_scalef32_pk_f16_fp8 v31, v31, 1.0 op_sel:[1,0,0]
	v_pk_fma_f16 v62, v4, v62, v24
	v_pk_fma_f16 v30, v4, v30, v25
	v_pk_fma_f16 v63, v4, v63, v26
	s_branch .Lic2_s69

.Lic2_s69:
	s_waitcnt vmcnt(4)
	v_cvt_scalef32_pk_f16_fp8 v64, v50, 1.0
	v_cvt_scalef32_pk_f16_fp8 v50, v50, 1.0 op_sel:[1,0,0]
	v_cvt_scalef32_pk_f16_fp8 v65, v51, 1.0
	v_cvt_scalef32_pk_f16_fp8 v51, v51, 1.0 op_sel:[1,0,0]
	v_pk_fma_f16 v31, v4, v31, v27
	s_waitcnt vmcnt(3)
	v_cvt_scalef32_pk_f16_fp8 v66, v52, 1.0
	v_cvt_scalef32_pk_f16_fp8 v52, v52, 1.0 op_sel:[1,0,0]
	v_cvt_scalef32_pk_f16_fp8 v67, v53, 1.0
	v_cvt_scalef32_pk_f16_fp8 v53, v53, 1.0 op_sel:[1,0,0]
	v_pk_fma_f16 v31, v4, v51, v31
	v_pk_fma_f16 v51, v4, v65, v63
	v_pk_fma_f16 v30, v4, v50, v30
	s_branch .Lic2_s70

.Lic2_s70:
	v_pk_fma_f16 v50, v4, v64, v62
	v_cvt_scalef32_pk_f16_fp8 v68, v54, 1.0
	v_cvt_scalef32_pk_f16_fp8 v54, v54, 1.0 op_sel:[1,0,0]
	v_cvt_scalef32_pk_f16_fp8 v69, v55, 1.0
	v_cvt_scalef32_pk_f16_fp8 v55, v55, 1.0 op_sel:[1,0,0]
	v_pk_fma_f16 v50, v4, v66, v50
	v_pk_fma_f16 v30, v4, v52, v30
	v_pk_fma_f16 v51, v4, v67, v51
	v_pk_fma_f16 v31, v4, v53, v31
	s_waitcnt vmcnt(1)
	v_cvt_scalef32_pk_f16_fp8 v70, v56, 1.0
	v_cvt_scalef32_pk_f16_fp8 v56, v56, 1.0 op_sel:[1,0,0]
	v_cvt_scalef32_pk_f16_fp8 v71, v57, 1.0
	v_cvt_scalef32_pk_f16_fp8 v57, v57, 1.0 op_sel:[1,0,0]
	s_branch .Lic2_s71

.Lic2_s71:
	v_pk_fma_f16 v31, v4, v55, v31
	v_pk_fma_f16 v51, v4, v69, v51
	v_pk_fma_f16 v30, v4, v54, v30
	v_pk_fma_f16 v50, v4, v68, v50
	v_cvt_scalef32_pk_f16_fp8 v72, v58, 1.0
	v_cvt_scalef32_pk_f16_fp8 v58, v58, 1.0 op_sel:[1,0,0]
	v_cvt_scalef32_pk_f16_fp8 v73, v59, 1.0
	v_cvt_scalef32_pk_f16_fp8 v59, v59, 1.0 op_sel:[1,0,0]
	v_pk_fma_f16 v50, v4, v70, v50
	v_pk_fma_f16 v30, v4, v56, v30
	v_pk_fma_f16 v51, v4, v71, v51
	v_pk_fma_f16 v31, v4, v57, v31
	s_waitcnt vmcnt(0)
	v_cvt_scalef32_pk_f16_fp8 v89, v28, 1.0
	s_branch .Lic2_s72

.Lic2_s72:
	v_cvt_scalef32_pk_f16_fp8 v28, v28, 1.0 op_sel:[1,0,0]
	v_cvt_scalef32_pk_f16_fp8 v90, v29, 1.0
	v_cvt_scalef32_pk_f16_fp8 v29, v29, 1.0 op_sel:[1,0,0]
	v_pk_fma_f16 v31, v4, v59, v31
	v_pk_fma_f16 v51, v4, v73, v51
	v_pk_fma_f16 v30, v4, v58, v30
	v_pk_fma_f16 v50, v4, v72, v50
	v_cvt_scalef32_pk_f16_fp8 v91, v60, 1.0
	v_cvt_scalef32_pk_f16_fp8 v60, v60, 1.0 op_sel:[1,0,0]
	v_cvt_scalef32_pk_f16_fp8 v92, v61, 1.0
	v_cvt_scalef32_pk_f16_fp8 v61, v61, 1.0 op_sel:[1,0,0]
	v_pk_fma_f16 v50, v4, v89, v50
	v_pk_fma_f16 v28, v4, v28, v30
	v_pk_fma_f16 v30, v4, v90, v51
	s_branch .Lic2_s73

.Lic2_s73:
	v_pk_fma_f16 v29, v4, v29, v31
	v_pk_fma_f16 v30, v4, v92, v30
	v_pk_fma_f16 v31, v4, v61, v29
	v_pk_fma_f16 v29, v4, v60, v28
	v_pk_fma_f16 v28, v4, v91, v50
.LBB5_80:
	s_waitcnt lgkmcnt(0)
	s_nop 0
	v_mov_b64_e32 v[24:25], v[28:29]
	v_mov_b64_e32 v[26:27], v[30:31]
	v_cmp_lt_i32_e32 vcc, s8, v87
	s_cbranch_vccz .LBB5_83
	v_add_u32_e32 v28, s8, v75
	v_cmp_lt_i32_e32 vcc, v28, v87
	v_mov_b32_e32 v28, 0x61a800
	s_branch .Lic2_s74

.Lic2_s74:
	s_and_saveexec_b64 s[6:7], vcc
	s_cbranch_execz .LBB5_79
	v_add_u32_e32 v28, s8, v5
	v_ashrrev_i32_e32 v29, 31, v28
	v_lshl_add_u64 v[28:29], v[28:29], 2, s[26:27]
	global_load_dword v28, v[28:29], off
	s_waitcnt vmcnt(0)
	v_lshlrev_b32_e32 v28, 6, v28
	v_and_b32_e32 v28, 0x7fffc0, v28
	s_branch .LBB5_79
.LBB5_83:
	s_cbranch_execz .LBB5_80
	ds_write_b128 v82, v[24:27]
	ds_read_b128 v[24:27], v83 offset:128
	ds_read_b128 v[28:31], v80
	s_branch .Lic2_s75

.Lic2_s75:
	ds_read_b128 v[50:53], v83 offset:8832
	s_waitcnt lgkmcnt(1)
	v_mfma_f32_16x16x32_f16 v[8:11], v[24:27], v[28:31], v[8:11]
	ds_read_b128 v[24:27], v83 offset:17536
	s_waitcnt lgkmcnt(1)
	v_mfma_f32_16x16x32_f16 v[12:15], v[50:53], v[28:31], v[12:15]
	s_waitcnt lgkmcnt(0)
	v_mfma_f32_16x16x32_f16 v[16:19], v[24:27], v[28:31], v[16:19]
	ds_read_b128 v[24:27], v83 offset:26240
	s_waitcnt lgkmcnt(0)
	v_mfma_f32_16x16x32_f16 v[20:23], v[24:27], v[28:31], v[20:23]
	ds_read_b128 v[24:27], v83 offset:192
	ds_read_b128 v[90:93], v80 offset:64
	ds_read_b128 v[28:31], v83 offset:8896
	s_branch .Lic2_s76

.Lic2_s76:
	ds_read_b128 v[94:97], v83 offset:17600
	s_waitcnt lgkmcnt(2)
	v_mfma_f32_16x16x32_f16 v[8:11], v[24:27], v[90:93], v[8:11]
	s_waitcnt lgkmcnt(1)
	v_mfma_f32_16x16x32_f16 v[12:15], v[28:31], v[90:93], v[12:15]
	v_add_u32_dpp v4, v88, v81 row_newbcast:0 row_mask:0xf bank_mask:0x3
	v_add_u32_dpp v4, v88, v81 row_newbcast:8 row_mask:0xf bank_mask:0xc
	v_add_u32_dpp v5, v88, v81 row_newbcast:1 row_mask:0xf bank_mask:0x3
	v_add_u32_dpp v5, v88, v81 row_newbcast:9 row_mask:0xf bank_mask:0xc
	v_add_u32_dpp v24, v88, v81 row_newbcast:2 row_mask:0xf bank_mask:0x3
	v_add_u32_dpp v24, v88, v81 row_newbcast:10 row_mask:0xf bank_mask:0xc
	v_add_u32_dpp v25, v88, v81 row_newbcast:3 row_mask:0xf bank_mask:0x3
	v_add_u32_dpp v25, v88, v81 row_newbcast:11 row_mask:0xf bank_mask:0xc
	global_load_dwordx2 v[70:71], v4, s[30:31]
	s_branch .Lic2_s77

.Lic2_s77:
	global_load_dwordx2 v[66:67], v5, s[30:31]
	global_load_dwordx2 v[62:63], v24, s[30:31]
	global_load_dwordx2 v[56:57], v25, s[30:31]
	v_add_u32_dpp v4, v88, v81 row_newbcast:4 row_mask:0xf bank_mask:0x3
	v_add_u32_dpp v4, v88, v81 row_newbcast:12 row_mask:0xf bank_mask:0xc
	v_add_u32_dpp v5, v88, v81 row_newbcast:5 row_mask:0xf bank_mask:0x3
	v_add_u32_dpp v5, v88, v81 row_newbcast:13 row_mask:0xf bank_mask:0xc
	v_add_u32_dpp v24, v88, v81 row_newbcast:6 row_mask:0xf bank_mask:0x3
	v_add_u32_dpp v24, v88, v81 row_newbcast:14 row_mask:0xf bank_mask:0xc
	v_add_u32_dpp v25, v88, v81 row_newbcast:7 row_mask:0xf bank_mask:0x3
	v_add_u32_dpp v25, v88, v81 row_newbcast:15 row_mask:0xf bank_mask:0xc
	global_load_dwordx2 v[68:69], v4, s[30:31]
	global_load_dwordx2 v[64:65], v5, s[30:31]
	global_load_dwordx2 v[58:59], v24, s[30:31]
	s_branch .Lic2_s78

.Lic2_s78:
	global_load_dwordx2 v[52:53], v25, s[30:31]
	v_add_u32_dpp v4, v86, v81 row_newbcast:0 row_mask:0xf bank_mask:0x3
	v_add_u32_dpp v4, v86, v81 row_newbcast:8 row_mask:0xf bank_mask:0xc
	v_add_u32_dpp v5, v86, v81 row_newbcast:1 row_mask:0xf bank_mask:0x3
	v_add_u32_dpp v5, v86, v81 row_newbcast:9 row_mask:0xf bank_mask:0xc
	v_add_u32_dpp v24, v86, v81 row_newbcast:2 row_mask:0xf bank_mask:0x3
	v_add_u32_dpp v24, v86, v81 row_newbcast:10 row_mask:0xf bank_mask:0xc
	v_add_u32_dpp v25, v86, v81 row_newbcast:3 row_mask:0xf bank_mask:0x3
	v_add_u32_dpp v25, v86, v81 row_newbcast:11 row_mask:0xf bank_mask:0xc
	global_load_dwordx2 v[60:61], v4, s[30:31]
	global_load_dwordx2 v[54:55], v5, s[30:31]
	global_load_dwordx2 v[50:51], v24, s[30:31]
	global_load_dwordx2 v[30:31], v25, s[30:31]
	v_add_u32_dpp v4, v86, v81 row_newbcast:4 row_mask:0xf bank_mask:0x3
	s_branch .Lic2_s79

.Lic2_s79:
	v_add_u32_dpp v4, v86, v81 row_newbcast:12 row_mask:0xf bank_mask:0xc
	v_add_u32_dpp v5, v86, v81 row_newbcast:5 row_mask:0xf bank_mask:0x3
	v_add_u32_dpp v5, v86, v81 row_newbcast:13 row_mask:0xf bank_mask:0xc
	v_add_u32_dpp v24, v86, v81 row_newbcast:6 row_mask:0xf bank_mask:0x3
	v_add_u32_dpp v24, v86, v81 row_newbcast:14 row_mask:0xf bank_mask:0xc
	v_add_u32_dpp v72, v86, v81 row_newbcast:7 row_mask:0xf bank_mask:0x3
	v_add_u32_dpp v72, v86, v81 row_newbcast:15 row_mask:0xf bank_mask:0xc
	global_load_dwordx2 v[28:29], v4, s[30:31]
	global_load_dwordx2 v[26:27], v5, s[30:31]
	s_nop 0
	global_load_dwordx2 v[24:25], v24, s[30:31]
	s_nop 0
	global_load_dwordx2 v[4:5], v72, s[30:31]
	ds_read_b128 v[86:89], v83 offset:26304
	s_branch .Lic2_s80

.Lic2_s80:
	s_waitcnt lgkmcnt(1)
	v_mfma_f32_16x16x32_f16 v[16:19], v[94:97], v[90:93], v[16:19]
	v_cmp_lt_i32_e32 vcc, 16, v85
	s_cmp_lg_u64 vcc, 0
	s_cselect_b64 s[36:37], -1, 0
	s_waitcnt lgkmcnt(0)
	v_mfma_f32_16x16x32_f16 v[20:23], v[86:89], v[90:93], v[20:23]
	v_cmp_lt_i32_e64 s[10:11], 18, v85
	v_cmp_lt_i32_e64 s[8:9], 20, v85
	v_cmp_lt_i32_e64 s[6:7], 22, v85
	s_cbranch_vccz .LBB5_86
	v_add_u32_dpp v34, v7, v81 row_newbcast:0 row_mask:0xf bank_mask:0x3
	v_add_u32_dpp v34, v7, v81 row_newbcast:8 row_mask:0xf bank_mask:0xc
	v_add_u32_dpp v38, v7, v81 row_newbcast:1 row_mask:0xf bank_mask:0x3
	s_branch .Lic2_s81

.Lic2_s81:
	v_add_u32_dpp v38, v7, v81 row_newbcast:9 row_mask:0xf bank_mask:0xc
	global_load_dwordx2 v[34:35], v34, s[30:31]
	s_nop 0
	global_load_dwordx2 v[38:39], v38, s[30:31]
.LBB5_86:
	s_cmp_lg_u64 s[10:11], 0
	s_cselect_b64 s[34:35], -1, 0
	s_cmp_eq_u64 s[10:11], 0
	s_cbranch_scc1 .LBB5_88
	v_add_u32_dpp v36, v7, v81 row_newbcast:2 row_mask:0xf bank_mask:0x3
	v_add_u32_dpp v36, v7, v81 row_newbcast:10 row_mask:0xf bank_mask:0xc
	v_add_u32_dpp v42, v7, v81 row_newbcast:3 row_mask:0xf bank_mask:0x3
	v_add_u32_dpp v42, v7, v81 row_newbcast:11 row_mask:0xf bank_mask:0xc
	global_load_dwordx2 v[36:37], v36, s[30:31]
	s_nop 0
	s_branch .Lic2_s82

.Lic2_s82:
	global_load_dwordx2 v[42:43], v42, s[30:31]

.LBB5_90:
	s_cmp_lg_u64 s[6:7], 0
	s_cselect_b64 s[8:9], -1, 0
	s_branch .Lic2_s83

.Lic2_s83:
	s_cmp_eq_u64 s[6:7], 0
	s_cbranch_scc1 .LBB5_92
	v_mov_b32_dpp v44, v7 row_newbcast:6 row_mask:0xf bank_mask:0x3
	v_mov_b32_dpp v44, v7 row_newbcast:14 row_mask:0xf bank_mask:0xc
	v_mov_b32_dpp v7, v7 row_newbcast:7 row_mask:0xf bank_mask:0x3
	s_nop 1
	v_mov_b32_dpp v7, v7 row_newbcast:15 row_mask:0xf bank_mask:0xc
	v_add_u32_e32 v44, v44, v81
	v_add_u32_e32 v7, v7, v81
	global_load_dwordx2 v[44:45], v44, s[30:31]
	s_nop 0
	global_load_dwordx2 v[48:49], v7, s[30:31]
.LBB5_92:
	v_cvt_f32_i32_e32 v7, v85
	s_waitcnt vmcnt(15)
	s_branch .Lic2_s84

.Lic2_s84:
	v_cvt_scalef32_pk_f16_fp8 v86, v70, 1.0
	v_cvt_scalef32_pk_f16_fp8 v70, v70, 1.0 op_sel:[1,0,0]
	v_max_f32_e32 v7, 1.0, v7
	v_div_scale_f32 v72, s[6:7], v7, v7, 1.0
	v_rcp_f32_e32 v73, v72
	v_div_scale_f32 v87, vcc, 1.0, v7, 1.0
	v_fma_f32 v88, -v72, v73, 1.0
	v_fmac_f32_e32 v73, v88, v73
	v_mul_f32_e32 v88, v87, v73
	v_fma_f32 v89, -v72, v88, v87
	v_fmac_f32_e32 v88, v89, v73
	v_fma_f32 v72, -v72, v88, v87
	v_div_fmas_f32 v72, v72, v73, v88
	v_div_fixup_f32 v7, v72, v7, 1.0
	s_branch .Lic2_s85

.Lic2_s85:
	v_mul_f32_e32 v72, 0x3c800000, v7
	v_fma_mixlo_f16 v7, v7, s29, 0
	v_cvt_scalef32_pk_f16_fp8 v73, v71, 1.0
	v_cvt_scalef32_pk_f16_fp8 v71, v71, 1.0 op_sel:[1,0,0]
	v_pk_fma_f16 v86, v7, v86, 0 op_sel_hi:[0,1,1]
	v_pk_fma_f16 v70, v7, v70, 0 op_sel_hi:[0,1,1]
	v_pk_fma_f16 v73, v7, v73, 0 op_sel_hi:[0,1,1]
	v_pk_fma_f16 v71, v7, v71, 0 op_sel_hi:[0,1,1]
	s_waitcnt vmcnt(14)
	v_cvt_scalef32_pk_f16_fp8 v87, v66, 1.0
	v_cvt_scalef32_pk_f16_fp8 v66, v66, 1.0 op_sel:[1,0,0]
	v_cvt_scalef32_pk_f16_fp8 v88, v67, 1.0
	v_cvt_scalef32_pk_f16_fp8 v67, v67, 1.0 op_sel:[1,0,0]
	v_pk_fma_f16 v67, v7, v67, v71 op_sel_hi:[0,1,1]
	s_branch .Lic2_s86

.Lic2_s86:
	v_pk_fma_f16 v71, v7, v88, v73 op_sel_hi:[0,1,1]
	v_pk_fma_f16 v66, v7, v66, v70 op_sel_hi:[0,1,1]
	v_pk_fma_f16 v70, v7, v87, v86 op_sel_hi:[0,1,1]
	s_waitcnt vmcnt(13)
	v_cvt_scalef32_pk_f16_fp8 v73, v62, 1.0
	v_cvt_scalef32_pk_f16_fp8 v62, v62, 1.0 op_sel:[1,0,0]
	v_cvt_scalef32_pk_f16_fp8 v86, v63, 1.0
	v_cvt_scalef32_pk_f16_fp8 v63, v63, 1.0 op_sel:[1,0,0]
	v_pk_fma_f16 v70, v7, v73, v70 op_sel_hi:[0,1,1]
	v_pk_fma_f16 v62, v7, v62, v66 op_sel_hi:[0,1,1]
	v_pk_fma_f16 v66, v7, v86, v71 op_sel_hi:[0,1,1]
	v_pk_fma_f16 v63, v7, v63, v67 op_sel_hi:[0,1,1]
	s_waitcnt vmcnt(12)
	v_cvt_scalef32_pk_f16_fp8 v67, v56, 1.0
	s_branch .Lic2_s87

.Lic2_s87:
	v_cvt_scalef32_pk_f16_fp8 v56, v56, 1.0 op_sel:[1,0,0]
	v_cvt_scalef32_pk_f16_fp8 v71, v57, 1.0
	v_cvt_scalef32_pk_f16_fp8 v57, v57, 1.0 op_sel:[1,0,0]
	v_pk_fma_f16 v57, v7, v57, v63 op_sel_hi:[0,1,1]
	v_pk_fma_f16 v63, v7, v71, v66 op_sel_hi:[0,1,1]
	v_pk_fma_f16 v56, v7, v56, v62 op_sel_hi:[0,1,1]
	v_pk_fma_f16 v62, v7, v67, v70 op_sel_hi:[0,1,1]
	s_waitcnt vmcnt(11)
	v_cvt_scalef32_pk_f16_fp8 v66, v68, 1.0
	v_cvt_scalef32_pk_f16_fp8 v67, v68, 1.0 op_sel:[1,0,0]
	v_cvt_scalef32_pk_f16_fp8 v68, v69, 1.0
	v_cvt_scalef32_pk_f16_fp8 v69, v69, 1.0 op_sel:[1,0,0]
	v_pk_fma_f16 v62, v7, v66, v62 op_sel_hi:[0,1,1]
	v_pk_fma_f16 v56, v7, v67, v56 op_sel_hi:[0,1,1]
	s_branch .Lic2_s88

.Lic2_s88:
	v_pk_fma_f16 v63, v7, v68, v63 op_sel_hi:[0,1,1]
	v_pk_fma_f16 v57, v7, v69, v57 op_sel_hi:[0,1,1]
	s_waitcnt vmcnt(10)
	v_cvt_scalef32_pk_f16_fp8 v66, v64, 1.0
	v_cvt_scalef32_pk_f16_fp8 v64, v64, 1.0 op_sel:[1,0,0]
	v_cvt_scalef32_pk_f16_fp8 v67, v65, 1.0
	v_cvt_scalef32_pk_f16_fp8 v65, v65, 1.0 op_sel:[1,0,0]
	v_pk_fma_f16 v57, v7, v65, v57 op_sel_hi:[0,1,1]
	v_pk_fma_f16 v63, v7, v67, v63 op_sel_hi:[0,1,1]
	v_pk_fma_f16 v56, v7, v64, v56 op_sel_hi:[0,1,1]
	v_pk_fma_f16 v62, v7, v66, v62 op_sel_hi:[0,1,1]
	s_waitcnt vmcnt(9)
	v_cvt_scalef32_pk_f16_fp8 v64, v58, 1.0
	v_cvt_scalef32_pk_f16_fp8 v58, v58, 1.0 op_sel:[1,0,0]
	s_branch .Lic2_s89

.Lic2_s89:
	v_cvt_scalef32_pk_f16_fp8 v65, v59, 1.0
	v_cvt_scalef32_pk_f16_fp8 v59, v59, 1.0 op_sel:[1,0,0]
	v_pk_fma_f16 v62, v7, v64, v62 op_sel_hi:[0,1,1]
	v_pk_fma_f16 v56, v7, v58, v56 op_sel_hi:[0,1,1]
	v_pk_fma_f16 v58, v7, v65, v63 op_sel_hi:[0,1,1]
	v_pk_fma_f16 v57, v7, v59, v57 op_sel_hi:[0,1,1]
	s_waitcnt vmcnt(8)
	v_cvt_scalef32_pk_f16_fp8 v59, v52, 1.0
	v_cvt_scalef32_pk_f16_fp8 v52, v52, 1.0 op_sel:[1,0,0]
	v_cvt_scalef32_pk_f16_fp8 v63, v53, 1.0
	v_cvt_scalef32_pk_f16_fp8 v53, v53, 1.0 op_sel:[1,0,0]
	v_pk_fma_f16 v53, v7, v53, v57 op_sel_hi:[0,1,1]
	v_pk_fma_f16 v57, v7, v63, v58 op_sel_hi:[0,1,1]
	v_pk_fma_f16 v52, v7, v52, v56 op_sel_hi:[0,1,1]
	s_branch .Lic2_s90

.Lic2_s90:
	v_pk_fma_f16 v56, v7, v59, v62 op_sel_hi:[0,1,1]
	s_waitcnt vmcnt(7)
	v_cvt_scalef32_pk_f16_fp8 v58, v60, 1.0
	v_cvt_scalef32_pk_f16_fp8 v59, v60, 1.0 op_sel:[1,0,0]
	v_cvt_scalef32_pk_f16_fp8 v60, v61, 1.0
	v_cvt_scalef32_pk_f16_fp8 v61, v61, 1.0 op_sel:[1,0,0]
	v_pk_fma_f16 v56, v7, v58, v56 op_sel_hi:[0,1,1]
	v_pk_fma_f16 v52, v7, v59, v52 op_sel_hi:[0,1,1]
	v_pk_fma_f16 v57, v7, v60, v57 op_sel_hi:[0,1,1]
	v_pk_fma_f16 v53, v7, v61, v53 op_sel_hi:[0,1,1]
	s_waitcnt vmcnt(6)
	v_cvt_scalef32_pk_f16_fp8 v58, v54, 1.0
	v_cvt_scalef32_pk_f16_fp8 v54, v54, 1.0 op_sel:[1,0,0]
	v_cvt_scalef32_pk_f16_fp8 v59, v55, 1.0
	s_branch .Lic2_s91

.Lic2_s91:
	v_cvt_scalef32_pk_f16_fp8 v55, v55, 1.0 op_sel:[1,0,0]
	v_pk_fma_f16 v53, v7, v55, v53 op_sel_hi:[0,1,1]
	v_pk_fma_f16 v55, v7, v59, v57 op_sel_hi:[0,1,1]
	v_pk_fma_f16 v52, v7, v54, v52 op_sel_hi:[0,1,1]
	v_pk_fma_f16 v54, v7, v58, v56 op_sel_hi:[0,1,1]
	s_waitcnt vmcnt(5)
	v_cvt_scalef32_pk_f16_fp8 v56, v50, 1.0
	v_cvt_scalef32_pk_f16_fp8 v50, v50, 1.0 op_sel:[1,0,0]
	v_cvt_scalef32_pk_f16_fp8 v57, v51, 1.0
	v_cvt_scalef32_pk_f16_fp8 v51, v51, 1.0 op_sel:[1,0,0]
	v_pk_fma_f16 v54, v7, v56, v54 op_sel_hi:[0,1,1]
	v_pk_fma_f16 v50, v7, v50, v52 op_sel_hi:[0,1,1]
	v_pk_fma_f16 v52, v7, v57, v55 op_sel_hi:[0,1,1]
	v_pk_fma_f16 v51, v7, v51, v53 op_sel_hi:[0,1,1]
	s_branch .Lic2_s92

.Lic2_s92:
	s_waitcnt vmcnt(4)
	v_cvt_scalef32_pk_f16_fp8 v53, v30, 1.0
	v_cvt_scalef32_pk_f16_fp8 v30, v30, 1.0 op_sel:[1,0,0]
	v_cvt_scalef32_pk_f16_fp8 v55, v31, 1.0
	v_cvt_scalef32_pk_f16_fp8 v31, v31, 1.0 op_sel:[1,0,0]
	v_pk_fma_f16 v31, v7, v31, v51 op_sel_hi:[0,1,1]
	v_pk_fma_f16 v51, v7, v55, v52 op_sel_hi:[0,1,1]
	v_pk_fma_f16 v30, v7, v30, v50 op_sel_hi:[0,1,1]
	v_pk_fma_f16 v50, v7, v53, v54 op_sel_hi:[0,1,1]
	s_waitcnt vmcnt(3)
	v_cvt_scalef32_pk_f16_fp8 v52, v28, 1.0
	v_cvt_scalef32_pk_f16_fp8 v28, v28, 1.0 op_sel:[1,0,0]
	v_cvt_scalef32_pk_f16_fp8 v53, v29, 1.0
	v_cvt_scalef32_pk_f16_fp8 v29, v29, 1.0 op_sel:[1,0,0]
	s_branch .Lic2_s93

.Lic2_s93:
	v_pk_fma_f16 v50, v7, v52, v50 op_sel_hi:[0,1,1]
	v_pk_fma_f16 v28, v7, v28, v30 op_sel_hi:[0,1,1]
	v_pk_fma_f16 v30, v7, v53, v51 op_sel_hi:[0,1,1]
	v_pk_fma_f16 v29, v7, v29, v31 op_sel_hi:[0,1,1]
	s_waitcnt vmcnt(2)
	v_cvt_scalef32_pk_f16_fp8 v31, v26, 1.0
	v_cvt_scalef32_pk_f16_fp8 v26, v26, 1.0 op_sel:[1,0,0]
	v_cvt_scalef32_pk_f16_fp8 v51, v27, 1.0
	v_cvt_scalef32_pk_f16_fp8 v27, v27, 1.0 op_sel:[1,0,0]
	v_pk_fma_f16 v27, v7, v27, v29 op_sel_hi:[0,1,1]
	v_pk_fma_f16 v29, v7, v51, v30 op_sel_hi:[0,1,1]
	v_pk_fma_f16 v26, v7, v26, v28 op_sel_hi:[0,1,1]
	v_pk_fma_f16 v28, v7, v31, v50 op_sel_hi:[0,1,1]
	s_waitcnt vmcnt(1)
	s_branch .Lic2_s94

.Lic2_s94:
	v_cvt_scalef32_pk_f16_fp8 v30, v24, 1.0
	v_cvt_scalef32_pk_f16_fp8 v24, v24, 1.0 op_sel:[1,0,0]
	v_cvt_scalef32_pk_f16_fp8 v31, v25, 1.0
	v_cvt_scalef32_pk_f16_fp8 v25, v25, 1.0 op_sel:[1,0,0]
	v_pk_fma_f16 v28, v7, v30, v28 op_sel_hi:[0,1,1]
	v_pk_fma_f16 v24, v7, v24, v26 op_sel_hi:[0,1,1]
	v_pk_fma_f16 v26, v7, v31, v29 op_sel_hi:[0,1,1]
	v_pk_fma_f16 v25, v7, v25, v27 op_sel_hi:[0,1,1]
	s_waitcnt vmcnt(0)
	v_cvt_scalef32_pk_f16_fp8 v29, v4, 1.0
	v_cvt_scalef32_pk_f16_fp8 v4, v4, 1.0 op_sel:[1,0,0]
	v_cvt_scalef32_pk_f16_fp8 v30, v5, 1.0
	v_cvt_scalef32_pk_f16_fp8 v5, v5, 1.0 op_sel:[1,0,0]
	v_cvt_pk_f16_f32 v72, v72, v72
	s_branch .Lic2_s95

.Lic2_s95:
	v_pk_fma_f16 v27, v7, v5, v25 op_sel_hi:[0,1,1]
	v_pk_fma_f16 v26, v7, v30, v26 op_sel_hi:[0,1,1]
	v_pk_fma_f16 v25, v7, v4, v24 op_sel_hi:[0,1,1]
	s_andn2_b64 vcc, exec, s[36:37]
	v_pk_fma_f16 v24, v7, v29, v28 op_sel_hi:[0,1,1]
	s_cbranch_vccnz .LBB5_94
	v_cvt_scalef32_pk_f16_fp8 v4, v34, 1.0
	v_cvt_scalef32_pk_f16_fp8 v5, v34, 1.0 op_sel:[1,0,0]
	v_cvt_scalef32_pk_f16_fp8 v7, v35, 1.0
	v_cvt_scalef32_pk_f16_fp8 v28, v35, 1.0 op_sel:[1,0,0]
	v_pk_fma_f16 v4, v72, v4, v24
	v_pk_fma_f16 v5, v72, v5, v25
	v_pk_fma_f16 v7, v72, v7, v26
	v_pk_fma_f16 v24, v72, v28, v27
	s_branch .Lic2_s96

.Lic2_s96:
	v_cvt_scalef32_pk_f16_fp8 v28, v38, 1.0
	v_cvt_scalef32_pk_f16_fp8 v25, v38, 1.0 op_sel:[1,0,0]
	v_cvt_scalef32_pk_f16_fp8 v26, v39, 1.0
	v_cvt_scalef32_pk_f16_fp8 v27, v39, 1.0 op_sel:[1,0,0]
	v_pk_fma_f16 v27, v72, v27, v24
	v_pk_fma_f16 v26, v72, v26, v7
	v_pk_fma_f16 v25, v72, v25, v5
	v_pk_fma_f16 v24, v72, v28, v4
.LBB5_94:
	s_andn2_b64 vcc, exec, s[34:35]
	s_cbranch_vccnz .LBB5_96
	v_cvt_scalef32_pk_f16_fp8 v4, v36, 1.0
	v_cvt_scalef32_pk_f16_fp8 v5, v36, 1.0 op_sel:[1,0,0]
	v_cvt_scalef32_pk_f16_fp8 v7, v37, 1.0
	v_cvt_scalef32_pk_f16_fp8 v28, v37, 1.0 op_sel:[1,0,0]
	s_branch .Lic2_s97

.Lic2_s97:
	v_pk_fma_f16 v4, v72, v4, v24
	v_pk_fma_f16 v5, v72, v5, v25
	v_pk_fma_f16 v7, v72, v7, v26
	v_pk_fma_f16 v24, v72, v28, v27
	v_cvt_scalef32_pk_f16_fp8 v28, v42, 1.0
	v_cvt_scalef32_pk_f16_fp8 v25, v42, 1.0 op_sel:[1,0,0]
	v_cvt_scalef32_pk_f16_fp8 v26, v43, 1.0
	v_cvt_scalef32_pk_f16_fp8 v27, v43, 1.0 op_sel:[1,0,0]
	v_pk_fma_f16 v27, v72, v27, v24
	v_pk_fma_f16 v26, v72, v26, v7
	v_pk_fma_f16 v25, v72, v25, v5
	v_pk_fma_f16 v24, v72, v28, v4
.LBB5_96:
	s_andn2_b64 vcc, exec, s[10:11]
	s_cbranch_vccnz .LBB5_98
	v_cvt_scalef32_pk_f16_fp8 v4, v40, 1.0
	s_branch .Lic2_s98

.Lic2_s98:
	v_cvt_scalef32_pk_f16_fp8 v5, v40, 1.0 op_sel:[1,0,0]
	v_cvt_scalef32_pk_f16_fp8 v7, v41, 1.0
	v_cvt_scalef32_pk_f16_fp8 v28, v41, 1.0 op_sel:[1,0,0]
	v_pk_fma_f16 v4, v72, v4, v24
	v_pk_fma_f16 v5, v72, v5, v25
	v_pk_fma_f16 v7, v72, v7, v26
	v_pk_fma_f16 v24, v72, v28, v27
	v_cvt_scalef32_pk_f16_fp8 v28, v46, 1.0
	v_cvt_scalef32_pk_f16_fp8 v25, v46, 1.0 op_sel:[1,0,0]
	v_cvt_scalef32_pk_f16_fp8 v26, v47, 1.0
	v_cvt_scalef32_pk_f16_fp8 v27, v47, 1.0 op_sel:[1,0,0]
	v_pk_fma_f16 v27, v72, v27, v24
	v_pk_fma_f16 v26, v72, v26, v7
	v_pk_fma_f16 v25, v72, v25, v5
	s_branch .Lic2_s99

.Lic2_s99:
	v_pk_fma_f16 v24, v72, v28, v4
.LBB5_98:
	s_andn2_b64 vcc, exec, s[8:9]
	s_cbranch_vccnz .LBB5_100
	v_cvt_scalef32_pk_f16_fp8 v4, v44, 1.0
	v_cvt_scalef32_pk_f16_fp8 v5, v44, 1.0 op_sel:[1,0,0]
	v_cvt_scalef32_pk_f16_fp8 v7, v45, 1.0
	v_cvt_scalef32_pk_f16_fp8 v28, v45, 1.0 op_sel:[1,0,0]
	v_pk_fma_f16 v4, v72, v4, v24
	v_pk_fma_f16 v5, v72, v5, v25
	v_pk_fma_f16 v7, v72, v7, v26
	v_pk_fma_f16 v24, v72, v28, v27
	v_cvt_scalef32_pk_f16_fp8 v28, v48, 1.0
	v_cvt_scalef32_pk_f16_fp8 v25, v48, 1.0 op_sel:[1,0,0]
	v_cvt_scalef32_pk_f16_fp8 v26, v49, 1.0
	s_branch .Lic2_s100

.Lic2_s100:
	v_cvt_scalef32_pk_f16_fp8 v27, v49, 1.0 op_sel:[1,0,0]
	v_pk_fma_f16 v27, v72, v27, v24
	v_pk_fma_f16 v26, v72, v26, v7
	v_pk_fma_f16 v25, v72, v25, v5
	v_pk_fma_f16 v24, v72, v28, v4

.LBB5_101:
	s_waitcnt lgkmcnt(0)
	s_or_b64 exec, exec, s[6:7]
	s_add_i32 s8, s8, 8
	v_add_u32_dpp v25, v24, v81 row_newbcast:0 row_mask:0xf bank_mask:0x3
	v_add_u32_dpp v25, v24, v81 row_newbcast:8 row_mask:0xf bank_mask:0xc
	v_add_u32_dpp v29, v24, v81 row_newbcast:1 row_mask:0xf bank_mask:0x3
	s_branch .Lic2_s101

.Lic2_s101:
	v_add_u32_dpp v29, v24, v81 row_newbcast:9 row_mask:0xf bank_mask:0xc
	global_load_dwordx2 v[26:27], v25, s[30:31]
	global_load_dwordx2 v[30:31], v29, s[30:31]
	v_add_u32_dpp v25, v24, v81 row_newbcast:2 row_mask:0xf bank_mask:0x3
	v_add_u32_dpp v25, v24, v81 row_newbcast:10 row_mask:0xf bank_mask:0xc
	v_add_u32_dpp v29, v24, v81 row_newbcast:3 row_mask:0xf bank_mask:0x3
	v_add_u32_dpp v29, v24, v81 row_newbcast:11 row_mask:0xf bank_mask:0xc
	global_load_dwordx2 v[50:51], v25, s[30:31]
	global_load_dwordx2 v[52:53], v29, s[30:31]
	v_add_u32_dpp v25, v24, v81 row_newbcast:4 row_mask:0xf bank_mask:0x3
	v_add_u32_dpp v25, v24, v81 row_newbcast:12 row_mask:0xf bank_mask:0xc
	v_add_u32_dpp v29, v24, v81 row_newbcast:5 row_mask:0xf bank_mask:0x3
	v_add_u32_dpp v29, v24, v81 row_newbcast:13 row_mask:0xf bank_mask:0xc
	global_load_dwordx2 v[54:55], v25, s[30:31]
	s_branch .Lic2_s102

.Lic2_s102:
	global_load_dwordx2 v[56:57], v29, s[30:31]
	v_mov_b32_dpp v25, v24 row_newbcast:6 row_mask:0xf bank_mask:0x3
	v_mov_b32_dpp v25, v24 row_newbcast:14 row_mask:0xf bank_mask:0xc
	v_mov_b32_dpp v29, v24 row_newbcast:7 row_mask:0xf bank_mask:0x3
	v_mov_b32_dpp v29, v24 row_newbcast:15 row_mask:0xf bank_mask:0xc
	v_add_u32_e32 v24, v25, v81
	global_load_dwordx2 v[24:25], v24, s[30:31]
	v_add_u32_e32 v29, v29, v81
	global_load_dwordx2 v[58:59], v29, s[30:31]
	s_waitcnt vmcnt(7)
	v_cvt_scalef32_pk_f16_fp8 v29, v26, 1.0
	v_cvt_scalef32_pk_f16_fp8 v26, v26, 1.0 op_sel:[1,0,0]
	v_cvt_scalef32_pk_f16_fp8 v60, v27, 1.0
	v_cvt_scalef32_pk_f16_fp8 v27, v27, 1.0 op_sel:[1,0,0]
	s_branch .Lic2_s103

.Lic2_s103:
	s_waitcnt vmcnt(6)
	v_cvt_scalef32_pk_f16_fp8 v61, v30, 1.0
	v_cvt_scalef32_pk_f16_fp8 v30, v30, 1.0 op_sel:[1,0,0]
	v_cvt_scalef32_pk_f16_fp8 v62, v31, 1.0
	v_cvt_scalef32_pk_f16_fp8 v31, v31, 1.0 op_sel:[1,0,0]
	v_pk_fma_f16 v29, v72, v29, v4
	v_pk_fma_f16 v26, v72, v26, v5
	v_pk_fma_f16 v60, v72, v60, v6
	v_pk_fma_f16 v27, v72, v27, v7
	s_waitcnt vmcnt(5)
	v_cvt_scalef32_pk_f16_fp8 v63, v50, 1.0
	v_cvt_scalef32_pk_f16_fp8 v50, v50, 1.0 op_sel:[1,0,0]
	v_cvt_scalef32_pk_f16_fp8 v64, v51, 1.0
	v_cvt_scalef32_pk_f16_fp8 v51, v51, 1.0 op_sel:[1,0,0]
	s_branch .Lic2_s104

.Lic2_s104:
	v_pk_fma_f16 v27, v72, v31, v27
	v_pk_fma_f16 v31, v72, v62, v60
	v_pk_fma_f16 v26, v72, v30, v26
	v_pk_fma_f16 v29, v72, v61, v29
	s_waitcnt vmcnt(4)
	v_cvt_scalef32_pk_f16_fp8 v65, v52, 1.0
	v_cvt_scalef32_pk_f16_fp8 v52, v52, 1.0 op_sel:[1,0,0]
	v_cvt_scalef32_pk_f16_fp8 v66, v53, 1.0
	v_cvt_scalef32_pk_f16_fp8 v53, v53, 1.0 op_sel:[1,0,0]
	v_pk_fma_f16 v29, v72, v63, v29
	v_pk_fma_f16 v26, v72, v50, v26
	v_pk_fma_f16 v30, v72, v64, v31
	v_pk_fma_f16 v27, v72, v51, v27
	s_waitcnt vmcnt(3)
	s_branch .Lic2_s105

.Lic2_s105:
	v_cvt_scalef32_pk_f16_fp8 v67, v54, 1.0
	v_cvt_scalef32_pk_f16_fp8 v54, v54, 1.0 op_sel:[1,0,0]
	v_cvt_scalef32_pk_f16_fp8 v68, v55, 1.0
	v_cvt_scalef32_pk_f16_fp8 v55, v55, 1.0 op_sel:[1,0,0]
	v_pk_fma_f16 v27, v72, v53, v27
	v_pk_fma_f16 v30, v72, v66, v30
	v_pk_fma_f16 v26, v72, v52, v26
	v_pk_fma_f16 v29, v72, v65, v29
	s_waitcnt vmcnt(2)
	v_cvt_scalef32_pk_f16_fp8 v69, v56, 1.0
	v_cvt_scalef32_pk_f16_fp8 v56, v56, 1.0 op_sel:[1,0,0]
	v_cvt_scalef32_pk_f16_fp8 v70, v57, 1.0
	v_cvt_scalef32_pk_f16_fp8 v57, v57, 1.0 op_sel:[1,0,0]
	v_pk_fma_f16 v29, v72, v67, v29
	s_branch .Lic2_s106

.Lic2_s106:
	v_pk_fma_f16 v26, v72, v54, v26
	v_pk_fma_f16 v30, v72, v68, v30
	v_pk_fma_f16 v27, v72, v55, v27
	s_waitcnt vmcnt(1)
	v_cvt_scalef32_pk_f16_fp8 v71, v24, 1.0
	v_cvt_scalef32_pk_f16_fp8 v24, v24, 1.0 op_sel:[1,0,0]
	v_cvt_scalef32_pk_f16_fp8 v73, v25, 1.0
	v_cvt_scalef32_pk_f16_fp8 v25, v25, 1.0 op_sel:[1,0,0]
	v_pk_fma_f16 v27, v72, v57, v27
	v_pk_fma_f16 v30, v72, v70, v30
	v_pk_fma_f16 v26, v72, v56, v26
	v_pk_fma_f16 v29, v72, v69, v29
	s_waitcnt vmcnt(0)
	v_cvt_scalef32_pk_f16_fp8 v86, v58, 1.0
	s_branch .Lic2_s107

.Lic2_s107:
	v_cvt_scalef32_pk_f16_fp8 v58, v58, 1.0 op_sel:[1,0,0]
	v_cvt_scalef32_pk_f16_fp8 v87, v59, 1.0
	v_cvt_scalef32_pk_f16_fp8 v59, v59, 1.0 op_sel:[1,0,0]
	v_pk_fma_f16 v29, v72, v71, v29
	v_pk_fma_f16 v24, v72, v24, v26
	v_pk_fma_f16 v26, v72, v73, v30
	v_pk_fma_f16 v25, v72, v25, v27
	v_pk_fma_f16 v26, v72, v87, v26
	v_pk_fma_f16 v27, v72, v59, v25
	v_pk_fma_f16 v25, v72, v58, v24
	v_pk_fma_f16 v24, v72, v86, v29
.LBB5_102:
	s_waitcnt lgkmcnt(0)
	s_nop 0
	v_mov_b64_e32 v[4:5], v[24:25]
	s_branch .Lic2_s108

.Lic2_s108:
	v_mov_b64_e32 v[6:7], v[26:27]
	v_cmp_lt_i32_e32 vcc, s8, v85
	s_cbranch_vccz .LBB5_105
	v_add_u32_e32 v24, s8, v75
	v_cmp_lt_i32_e32 vcc, v24, v85
	v_mov_b32_e32 v24, 0x61a800
	s_and_saveexec_b64 s[6:7], vcc
	s_cbranch_execz .LBB5_101
	v_add_u32_e32 v24, s8, v28
	v_ashrrev_i32_e32 v25, 31, v24
	v_lshl_add_u64 v[24:25], v[24:25], 2, s[26:27]
	global_load_dword v24, v[24:25], off
	s_waitcnt vmcnt(0)
	v_lshlrev_b32_e32 v24, 6, v24
	s_branch .Lic2_s109

.Lic2_s109:
	v_and_b32_e32 v24, 0x7fffc0, v24
	s_branch .LBB5_101
.LBB5_105:
	s_cbranch_execz .LBB5_102
	ds_write_b128 v82, v[4:7]
	ds_read_b128 v[4:7], v83 offset:256
	ds_read_b128 v[24:27], v80
	ds_read_b128 v[28:31], v83 offset:8960
	s_waitcnt lgkmcnt(1)
	v_mfma_f32_16x16x32_f16 v[4:7], v[4:7], v[24:27], v[8:11]
	s_nop 2
	ds_read_b128 v[8:11], v83 offset:17664
	s_waitcnt lgkmcnt(1)
	v_mfma_f32_16x16x32_f16 v[12:15], v[28:31], v[24:27], v[12:15]
	s_waitcnt lgkmcnt(0)
	s_branch .Lic2_s110

.Lic2_s110:
	v_mfma_f32_16x16x32_f16 v[8:11], v[8:11], v[24:27], v[16:19]
	s_nop 2
	ds_read_b128 v[16:19], v83 offset:26368
	s_waitcnt lgkmcnt(0)
	v_mfma_f32_16x16x32_f16 v[16:19], v[16:19], v[24:27], v[20:23]
	s_nop 2
	ds_read_b128 v[20:23], v83 offset:320
	ds_read_b128 v[24:27], v80 offset:64
	ds_read_b128 v[28:31], v83 offset:9024
	s_waitcnt lgkmcnt(1)
	v_mfma_f32_16x16x32_f16 v[4:7], v[20:23], v[24:27], v[4:7]
	ds_read_b128 v[20:23], v83 offset:17728
	s_waitcnt lgkmcnt(1)
	v_mfma_f32_16x16x32_f16 v[12:15], v[28:31], v[24:27], v[12:15]
	s_branch .Lic2_s111

.Lic2_s111:
	s_waitcnt lgkmcnt(0)
	v_mfma_f32_16x16x32_f16 v[8:11], v[20:23], v[24:27], v[8:11]
	ds_read_b128 v[20:23], v83 offset:26432
	ds_write_b128 v82, v[0:3]
	s_waitcnt lgkmcnt(1)
	v_mfma_f32_16x16x32_f16 v[0:3], v[20:23], v[24:27], v[16:19]
	s_nop 2
	ds_read_b128 v[16:19], v83 offset:384
	ds_read_b128 v[20:23], v80
	ds_read_b128 v[24:27], v83 offset:9088
	s_waitcnt lgkmcnt(1)
	v_mfma_f32_16x16x32_f16 v[4:7], v[16:19], v[20:23], v[4:7]
	ds_read_b128 v[16:19], v83 offset:17792
	s_waitcnt lgkmcnt(1)
	s_branch .Lic2_s112

.Lic2_s112:
	v_mfma_f32_16x16x32_f16 v[12:15], v[24:27], v[20:23], v[12:15]
	s_waitcnt lgkmcnt(0)
	v_mfma_f32_16x16x32_f16 v[8:11], v[16:19], v[20:23], v[8:11]
	ds_read_b128 v[16:19], v83 offset:26496
	s_waitcnt lgkmcnt(0)
	v_mfma_f32_16x16x32_f16 v[0:3], v[16:19], v[20:23], v[0:3]
	ds_read_b128 v[16:19], v83 offset:448
	ds_read_b128 v[20:23], v80 offset:64
	ds_read_b128 v[24:27], v83 offset:9152
	ds_read_b128 v[28:31], v83 offset:17856
	ds_read_b128 v[50:53], v83 offset:26560
	s_mov_b64 s[6:7], s[22:23]
	s_mov_b64 s[8:9], s[18:19]
	s_waitcnt lgkmcnt(1)
	s_branch .Lic2_s113

.Lic2_s113:
	v_mfma_f32_16x16x32_f16 v[8:11], v[28:31], v[20:23], v[8:11]
	s_nop 0
	s_waitcnt lgkmcnt(0)
	v_mfma_f32_16x16x32_f16 v[0:3], v[50:53], v[20:23], v[0:3]
	v_mfma_f32_16x16x32_f16 v[16:19], v[16:19], v[20:23], v[4:7]
	s_nop 2
	v_add_u32_e32 v6, s33, v77
	v_mfma_f32_16x16x32_f16 v[12:15], v[24:27], v[20:23], v[12:15]
	v_cmp_gt_i32_e32 vcc, s28, v6
	ds_read_b128 v[20:23], v32 offset:52240
	ds_read_b128 v[24:27], v32 offset:52496
	ds_read_b128 v[28:31], v32 offset:52752
	s_waitcnt lgkmcnt(2)
	v_add_f32_e32 v7, v16, v20
	s_branch .Lic2_s114

.Lic2_s114:
	s_waitcnt lgkmcnt(1)
	v_mov_b32_e32 v4, v24
	s_waitcnt lgkmcnt(0)
	v_mov_b32_e32 v5, v28
	v_add_f32_e32 v16, v17, v21
	v_add_f32_e32 v17, v18, v22
	v_add_f32_e32 v18, v19, v23
	v_max_f32_e32 v24, 0, v7
	v_max_f32_e32 v62, 0, v16
	v_max_f32_e32 v64, 0, v17
	v_max_f32_e32 v66, 0, v18
	ds_read_b128 v[16:19], v32 offset:52304
	ds_read_b128 v[20:23], v32 offset:52560
	ds_read_b128 v[50:53], v32 offset:52816
	s_branch .Lic2_s115

.Lic2_s115:
	s_waitcnt lgkmcnt(2)
	v_add_f32_e32 v7, v12, v16
	v_add_f32_e32 v12, v13, v17
	v_add_f32_e32 v13, v14, v18
	v_add_f32_e32 v14, v15, v19
	v_max_f32_e32 v68, 0, v7
	v_max_f32_e32 v70, 0, v12
	v_max_f32_e32 v72, 0, v13
	v_max_f32_e32 v86, 0, v14
	ds_read_b128 v[12:15], v32 offset:52368
	ds_read_b128 v[16:19], v32 offset:52624
	ds_read_b128 v[54:57], v32 offset:52880
	v_pk_fma_f32 v[88:89], v[4:5], v[24:25], 0 op_sel_hi:[1,0,0]
	v_mov_b32_e32 v28, v25
	s_branch .Lic2_s116

.Lic2_s116:
	v_mov_b32_e32 v24, v26
	v_mov_b32_e32 v25, v30
	v_mov_b32_e32 v30, v27
	s_waitcnt lgkmcnt(4)
	v_mov_b32_e32 v26, v20
	s_waitcnt lgkmcnt(3)
	v_mov_b32_e32 v27, v50
	v_mov_b32_e32 v50, v21
	v_mov_b32_e32 v20, v22
	v_mov_b32_e32 v21, v52
	v_mov_b32_e32 v52, v23
	v_pk_fma_f32 v[22:23], v[28:29], v[62:63], v[88:89] op_sel_hi:[1,0,1]
	v_mov_b32_e32 v4, v33
	v_pk_fma_f32 v[22:23], v[24:25], v[64:65], v[22:23] op_sel_hi:[1,0,1]
	s_branch .Lic2_s117

.Lic2_s117:
	v_mov_b32_e32 v5, v33
	v_pk_fma_f32 v[22:23], v[30:31], v[66:67], v[22:23] op_sel_hi:[1,0,1]
	s_waitcnt lgkmcnt(2)
	v_add_f32_e32 v7, v8, v12
	v_pk_fma_f32 v[22:23], v[26:27], v[68:69], v[22:23] op_sel_hi:[1,0,1]
	s_waitcnt lgkmcnt(1)
	v_mov_b32_e32 v8, v16
	v_pk_fma_f32 v[22:23], v[50:51], v[70:71], v[22:23] op_sel_hi:[1,0,1]
	v_add_f32_e32 v11, v11, v15
	v_pk_fma_f32 v[20:21], v[20:21], v[72:73], v[22:23] op_sel_hi:[1,0,1]
	v_add_f32_e32 v22, v9, v13
	v_pk_fma_f32 v[20:21], v[52:53], v[86:87], v[20:21] op_sel_hi:[1,0,1]
	v_add_f32_e32 v23, v10, v14
	s_waitcnt lgkmcnt(0)
	s_branch .Lic2_s118

.Lic2_s118:
	v_mov_b32_e32 v9, v54
	v_max_f32_e32 v10, 0, v7
	v_mov_b32_e32 v54, v17
	v_max_f32_e32 v14, 0, v22
	v_pk_fma_f32 v[8:9], v[8:9], v[10:11], v[20:21] op_sel_hi:[1,0,1]
	v_mov_b32_e32 v12, v18
	v_mov_b32_e32 v13, v56
	v_max_f32_e32 v16, 0, v23
	v_pk_fma_f32 v[8:9], v[54:55], v[14:15], v[8:9] op_sel_hi:[1,0,1]
	v_max_f32_e32 v22, 0, v11
	v_pk_fma_f32 v[8:9], v[12:13], v[16:17], v[8:9] op_sel_hi:[1,0,1]
	v_mov_b32_e32 v56, v19
	ds_read_b128 v[10:13], v32 offset:52432
	ds_read_b128 v[14:17], v32 offset:52688
	s_branch .Lic2_s119

.Lic2_s119:
	ds_read_b128 v[18:21], v32 offset:52944
	v_pk_fma_f32 v[22:23], v[56:57], v[22:23], v[8:9] op_sel_hi:[1,0,1]
	v_and_b32_e32 v24, 64, v84
	v_xor_b32_e32 v7, 16, v84
	v_add_u32_e32 v8, 64, v24
	v_cmp_lt_i32_e64 s[6:7], v7, v8
	s_and_b64 s[8:9], s[2:3], vcc
	s_waitcnt lgkmcnt(2)
	v_add_f32_e32 v9, v0, v10
	v_add_f32_e32 v11, v1, v11
	s_waitcnt lgkmcnt(1)
	v_mov_b32_e32 v0, v14
	s_waitcnt lgkmcnt(0)
	v_mov_b32_e32 v1, v18
	s_branch .Lic2_s120

.Lic2_s120:
	v_max_f32_e32 v10, 0, v9
	v_add_f32_e32 v24, v2, v12
	v_add_f32_e32 v13, v3, v13
	v_mov_b32_e32 v18, v15
	v_max_f32_e32 v12, 0, v11
	v_pk_fma_f32 v[0:1], v[0:1], v[10:11], v[22:23] op_sel_hi:[1,0,1]
	v_mov_b32_e32 v2, v16
	v_mov_b32_e32 v3, v20
	v_max_f32_e32 v14, 0, v24
	v_pk_fma_f32 v[0:1], v[18:19], v[12:13], v[0:1] op_sel_hi:[1,0,1]
	v_cndmask_b32_e64 v7, v84, v7, s[6:7]
	v_mov_b32_e32 v20, v17
	v_max_f32_e32 v16, 0, v13
	v_pk_fma_f32 v[0:1], v[2:3], v[14:15], v[0:1] op_sel_hi:[1,0,1]
	s_branch .Lic2_s121

.Lic2_s121:
	v_lshlrev_b32_e32 v7, 2, v7
	v_pk_fma_f32 v[0:1], v[20:21], v[16:17], v[0:1] op_sel_hi:[1,0,1]
	ds_bpermute_b32 v2, v7, v0
	ds_bpermute_b32 v3, v7, v1
	v_xor_b32_e32 v7, 32, v84
	v_cmp_lt_i32_e64 s[6:7], v7, v8
	v_mov_b32_e32 v10, -1
	s_waitcnt lgkmcnt(0)
	v_pk_add_f32 v[0:1], v[0:1], v[2:3]
	v_cndmask_b32_e64 v7, v84, v7, s[6:7]
	v_lshlrev_b32_e32 v7, 2, v7
	ds_bpermute_b32 v2, v7, v0
	ds_bpermute_b32 v3, v7, v1
	v_mov_b32_e32 v7, 0
	s_branch .Lic2_s122

.Lic2_s122:
	s_and_saveexec_b64 s[6:7], s[8:9]
	s_cbranch_execz .LBB5_108
	v_mov_b32_e32 v10, v103
	s_waitcnt lgkmcnt(0)
	v_pk_add_f32 v[4:5], v[0:1], v[2:3]
	v_mov_b32_e32 v7, 1.0
.LBB5_108:
	s_or_b64 exec, exec, s[6:7]
	v_lshlrev_b32_e32 v0, 2, v84
	v_and_b32_e32 v0, 0x100, v0
	ds_bpermute_b32 v9, v0, v10
	s_xor_b64 s[10:11], s[8:9], -1
	s_waitcnt lgkmcnt(0)
	v_cmp_eq_u32_e32 vcc, v10, v9
	s_or_b64 s[10:11], vcc, s[10:11]
	s_branch .Lic2_s123

.Lic2_s123:
	v_cndmask_b32_e64 v0, 0, 1, s[10:11]
	v_cmp_ne_u32_e32 vcc, 0, v0
	s_cmp_lg_u64 vcc, exec
	v_cmp_gt_i32_e64 s[6:7], 0, v9
	s_cselect_b64 s[10:11], -1, 0
	s_or_b64 s[10:11], s[6:7], s[10:11]
	s_mov_b64 s[6:7], 0
	s_and_saveexec_b64 s[34:35], s[10:11]
	s_xor_b64 s[10:11], exec, s[34:35]
	s_cbranch_execnz .LBB5_111
	s_or_saveexec_b64 s[8:9], s[10:11]
	v_mov_b32_e32 v10, 1.0
	s_xor_b64 exec, exec, s[8:9]
	s_cbranch_execnz .LBB5_114
.LBB5_110:
	s_waitcnt lgkmcnt(0)
	s_branch .Lic2_s124

.LBB5_111:
	s_and_b64 s[8:9], s[4:5], s[8:9]
	s_and_saveexec_b64 s[34:35], s[8:9]
	s_xor_b64 s[8:9], exec, s[34:35]
	v_lshlrev_b32_e32 v0, 2, v10
	s_mov_b64 s[6:7], exec
	v_ashrrev_i32_e32 v1, 31, v0
	s_or_b64 exec, exec, s[8:9]
	s_and_b64 s[6:7], s[6:7], exec
	s_or_saveexec_b64 s[8:9], s[10:11]
	s_branch .Lic2_s125

.Lic2_s125:
	v_mov_b32_e32 v10, 1.0
	s_xor_b64 exec, exec, s[8:9]
	s_cbranch_execz .LBB5_110
.LBB5_114:
	v_xor_b32_e32 v0, 1, v84
	v_cmp_lt_i32_e32 vcc, v0, v8
	v_xor_b32_e32 v3, 2, v84
	s_mov_b64 s[10:11], s[6:7]
	v_cndmask_b32_e32 v0, v84, v0, vcc
	v_lshlrev_b32_e32 v1, 2, v0
	ds_bpermute_b32 v2, v1, v7
	ds_bpermute_b32 v0, v1, v4
	ds_bpermute_b32 v1, v1, v5
	v_cmp_lt_i32_e32 vcc, v3, v8
	s_waitcnt lgkmcnt(2)
	s_branch .Lic2_s126

.Lic2_s126:
	v_add_f32_e32 v6, v7, v2
	v_cndmask_b32_e32 v2, v84, v3, vcc
	v_lshlrev_b32_e32 v7, 2, v2
	s_waitcnt lgkmcnt(0)
	v_pk_add_f32 v[0:1], v[4:5], v[0:1]
	ds_bpermute_b32 v2, v7, v0
	ds_bpermute_b32 v3, v7, v1
	ds_bpermute_b32 v4, v7, v6
	s_waitcnt lgkmcnt(1)
	v_pk_add_f32 v[2:3], v[0:1], v[2:3]
	v_xor_b32_e32 v0, 4, v84
	v_cmp_lt_i32_e32 vcc, v0, v8
	s_waitcnt lgkmcnt(0)
	v_add_f32_e32 v11, v6, v4
	v_cndmask_b32_e32 v0, v84, v0, vcc
	s_branch .Lic2_s127

.Lic2_s127:
	v_lshlrev_b32_e32 v0, 2, v0
	ds_bpermute_b32 v6, v0, v2
	ds_bpermute_b32 v7, v0, v3
	ds_bpermute_b32 v8, v0, v11
	s_and_saveexec_b64 s[34:35], s[0:1]
	s_cbranch_execz .LBB5_116
	s_waitcnt lgkmcnt(0)
	v_add_f32_e32 v10, v11, v8
	v_pk_add_f32 v[4:5], v[2:3], v[6:7]
	v_lshlrev_b32_e32 v0, 2, v9
	v_mov_b32_e32 v1, v33
	s_or_b64 s[10:11], s[6:7], exec
.LBB5_116:
	s_or_b64 exec, exec, s[34:35]
	s_andn2_b64 s[6:7], s[6:7], exec
	s_branch .Lic2_s128

.Lic2_s128:
	s_and_b64 s[10:11], s[10:11], exec
	s_or_b64 s[6:7], s[6:7], s[10:11]
	s_or_b64 exec, exec, s[8:9]
	s_and_saveexec_b64 s[8:9], s[6:7]
	s_xor_b64 s[6:7], exec, s[8:9]
	s_cbranch_execz .LBB5_11
